# P7 gather: no refills past the last row of a token (tail re-reads removed, counted waits shrink over the last rows)
# speedup vs baseline: 1.0385x; 1.0187x over previous
; DI void peer_token(LAS unsigned char* ring, const bf16* x1row, float inv2, const float* nffn, const int* ex, const float* pg, const unsigned char* U6, const unsigned char* V6,
;                    const float* usc, const float* vsc, float* orow, int lane) {
;     ...
;     for (int k = 64; k < 120; ++k) P11_V(k, cf_hi, vl, e_hi, k - 56);
; #pragma unroll 1
;     for (int k = 120; k < 128; ++k) P11_V(k, cf_hi, vl, e_lo, k - 120);
.Lv_sweep_hi:
	s_add_i32 s47, s46, 1
	s_and_b32 s47, s47, 7
	s_lshl_b32 s47, s47, 11
	s_add_i32 s77, s33, s47
	v_add_u32_e32 v4, s77, v70
	s_add_i32 s78, s46, 9
	s_and_b32 s75, s78, 0x7f
	v_readlane_b32 s79, v113, s75
	v_readlane_b32 s47, v112, s75
	s_bitcmp1_b32 s75, 6
	s_cselect_b32 s47, s79, s47
	s_lshl_b32 s47, s47, 11
	s_bitcmp1_b32 s78, 7
	s_cselect_b32 s78, s98, 0
	s_cselect_b32 s79, s99, 0
	s_add_u32 s78, s78, s47
	s_addc_u32 s79, s79, 0
	v_readlane_b32 s74, v125, s46
	s_waitcnt vmcnt(14)
	ds_read_b128 v[126:129], v4
	ds_read_b128 v[130:133], v4 offset:1024
	v_lshl_add_u64 v[2:3], v[72:73], 0, s[78:79]
	v_cvt_scalef32_pk_f32_fp4 v[136:137], v98, 1.0
	v_cvt_scalef32_pk_f32_fp4 v[138:139], v98, 1.0 op_sel:[1,0,0]
	v_cvt_scalef32_pk_f32_fp4 v[140:141], v98, 1.0 op_sel:[0,1,0]
	v_cvt_scalef32_pk_f32_fp4 v[142:143], v98, 1.0 op_sel:[1,1,0]
	v_pk_fma_f32 v[94:95], s[74:75], v[136:137], v[94:95] op_sel_hi:[0,1,1]
	v_pk_fma_f32 v[96:97], s[74:75], v[138:139], v[96:97] op_sel_hi:[0,1,1]
	v_pk_fma_f32 v[92:93], s[74:75], v[140:141], v[92:93] op_sel_hi:[0,1,1]
	v_pk_fma_f32 v[90:91], s[74:75], v[142:143], v[90:91] op_sel_hi:[0,1,1]
	v_cvt_scalef32_pk_f32_fp4 v[136:137], v99, 1.0
	v_cvt_scalef32_pk_f32_fp4 v[138:139], v99, 1.0 op_sel:[1,0,0]
	v_cvt_scalef32_pk_f32_fp4 v[140:141], v99, 1.0 op_sel:[0,1,0]
	v_cvt_scalef32_pk_f32_fp4 v[142:143], v99, 1.0 op_sel:[1,1,0]
	v_pk_fma_f32 v[88:89], s[74:75], v[136:137], v[88:89] op_sel_hi:[0,1,1]
	v_pk_fma_f32 v[86:87], s[74:75], v[138:139], v[86:87] op_sel_hi:[0,1,1]
	v_pk_fma_f32 v[84:85], s[74:75], v[140:141], v[84:85] op_sel_hi:[0,1,1]
	v_pk_fma_f32 v[82:83], s[74:75], v[142:143], v[82:83] op_sel_hi:[0,1,1]
	v_cvt_scalef32_pk_f32_fp4 v[136:137], v100, 1.0
	v_cvt_scalef32_pk_f32_fp4 v[138:139], v100, 1.0 op_sel:[1,0,0]
	v_cvt_scalef32_pk_f32_fp4 v[140:141], v100, 1.0 op_sel:[0,1,0]
	v_cvt_scalef32_pk_f32_fp4 v[142:143], v100, 1.0 op_sel:[1,1,0]
	v_pk_fma_f32 v[64:65], s[74:75], v[136:137], v[64:65] op_sel_hi:[0,1,1]
	v_pk_fma_f32 v[80:81], s[74:75], v[138:139], v[80:81] op_sel_hi:[0,1,1]
	v_pk_fma_f32 v[62:63], s[74:75], v[140:141], v[62:63] op_sel_hi:[0,1,1]
	v_pk_fma_f32 v[60:61], s[74:75], v[142:143], v[60:61] op_sel_hi:[0,1,1]
	s_waitcnt lgkmcnt(0)
	s_mov_b32 m0, s77
	s_nop 0
	global_load_lds_dwordx4 v[2:3], off
	global_load_lds_dwordx4 v[2:3], off offset:1024
	v_cvt_scalef32_pk_f32_fp4 v[136:137], v101, 1.0
	v_cvt_scalef32_pk_f32_fp4 v[138:139], v101, 1.0 op_sel:[1,0,0]
	v_cvt_scalef32_pk_f32_fp4 v[140:141], v101, 1.0 op_sel:[0,1,0]
	v_cvt_scalef32_pk_f32_fp4 v[142:143], v101, 1.0 op_sel:[1,1,0]
	v_pk_fma_f32 v[58:59], s[74:75], v[136:137], v[58:59] op_sel_hi:[0,1,1]
	v_pk_fma_f32 v[56:57], s[74:75], v[138:139], v[56:57] op_sel_hi:[0,1,1]
	v_pk_fma_f32 v[54:55], s[74:75], v[140:141], v[54:55] op_sel_hi:[0,1,1]
	v_pk_fma_f32 v[52:53], s[74:75], v[142:143], v[52:53] op_sel_hi:[0,1,1]
	v_cvt_scalef32_pk_f32_fp4 v[136:137], v102, 1.0
	v_cvt_scalef32_pk_f32_fp4 v[138:139], v102, 1.0 op_sel:[1,0,0]
	v_cvt_scalef32_pk_f32_fp4 v[140:141], v102, 1.0 op_sel:[0,1,0]
	v_cvt_scalef32_pk_f32_fp4 v[142:143], v102, 1.0 op_sel:[1,1,0]
	v_pk_fma_f32 v[50:51], s[74:75], v[136:137], v[50:51] op_sel_hi:[0,1,1]
	v_pk_fma_f32 v[48:49], s[74:75], v[138:139], v[48:49] op_sel_hi:[0,1,1]
	v_pk_fma_f32 v[46:47], s[74:75], v[140:141], v[46:47] op_sel_hi:[0,1,1]
	v_pk_fma_f32 v[44:45], s[74:75], v[142:143], v[44:45] op_sel_hi:[0,1,1]
	v_cvt_scalef32_pk_f32_fp4 v[136:137], v103, 1.0
	v_cvt_scalef32_pk_f32_fp4 v[138:139], v103, 1.0 op_sel:[1,0,0]
	v_cvt_scalef32_pk_f32_fp4 v[140:141], v103, 1.0 op_sel:[0,1,0]
	v_cvt_scalef32_pk_f32_fp4 v[142:143], v103, 1.0 op_sel:[1,1,0]
	v_pk_fma_f32 v[42:43], s[74:75], v[136:137], v[42:43] op_sel_hi:[0,1,1]
	v_pk_fma_f32 v[40:41], s[74:75], v[138:139], v[40:41] op_sel_hi:[0,1,1]
	v_pk_fma_f32 v[38:39], s[74:75], v[140:141], v[38:39] op_sel_hi:[0,1,1]
	v_pk_fma_f32 v[36:37], s[74:75], v[142:143], v[36:37] op_sel_hi:[0,1,1]
	v_cvt_scalef32_pk_f32_fp4 v[136:137], v104, 1.0
	v_cvt_scalef32_pk_f32_fp4 v[138:139], v104, 1.0 op_sel:[1,0,0]
	v_cvt_scalef32_pk_f32_fp4 v[140:141], v104, 1.0 op_sel:[0,1,0]
	v_cvt_scalef32_pk_f32_fp4 v[142:143], v104, 1.0 op_sel:[1,1,0]
	v_pk_fma_f32 v[32:33], s[74:75], v[136:137], v[32:33] op_sel_hi:[0,1,1]
	v_pk_fma_f32 v[34:35], s[74:75], v[138:139], v[34:35] op_sel_hi:[0,1,1]
	v_pk_fma_f32 v[30:31], s[74:75], v[140:141], v[30:31] op_sel_hi:[0,1,1]
	v_pk_fma_f32 v[28:29], s[74:75], v[142:143], v[28:29] op_sel_hi:[0,1,1]
	v_cvt_scalef32_pk_f32_fp4 v[136:137], v105, 1.0
	v_cvt_scalef32_pk_f32_fp4 v[138:139], v105, 1.0 op_sel:[1,0,0]
	v_cvt_scalef32_pk_f32_fp4 v[140:141], v105, 1.0 op_sel:[0,1,0]
	v_cvt_scalef32_pk_f32_fp4 v[142:143], v105, 1.0 op_sel:[1,1,0]
	v_pk_fma_f32 v[26:27], s[74:75], v[136:137], v[26:27] op_sel_hi:[0,1,1]
	v_pk_fma_f32 v[24:25], s[74:75], v[138:139], v[24:25] op_sel_hi:[0,1,1]
	v_pk_fma_f32 v[20:21], s[74:75], v[140:141], v[20:21] op_sel_hi:[0,1,1]
	v_pk_fma_f32 v[22:23], s[74:75], v[142:143], v[22:23] op_sel_hi:[0,1,1]
	s_add_i32 s47, s46, 2
	s_and_b32 s47, s47, 7
	s_lshl_b32 s47, s47, 11
	s_add_i32 s77, s33, s47
	v_add_u32_e32 v4, s77, v70
	s_add_i32 s78, s46, 10
	s_and_b32 s75, s78, 0x7f
	v_readlane_b32 s79, v113, s75
	v_readlane_b32 s47, v112, s75
	s_bitcmp1_b32 s75, 6
	s_cselect_b32 s47, s79, s47
	s_lshl_b32 s47, s47, 11
	s_bitcmp1_b32 s78, 7
	s_cselect_b32 s78, s98, 0
	s_cselect_b32 s79, s99, 0
	s_add_u32 s78, s78, s47
	s_addc_u32 s79, s79, 0
	s_add_i32 s32, s46, 1
	v_readlane_b32 s74, v125, s32
	s_waitcnt vmcnt(14)
; DI void peer_token(LAS unsigned char* ring, const bf16* x1row, float inv2, const float* nffn, const int* ex, const float* pg, const unsigned char* U6, const unsigned char* V6,
;                    const float* usc, const float* vsc, float* orow, int lane) {
;     ...
;     for (int k = 64; k < 120; ++k) P11_V(k, cf_hi, vl, e_hi, k - 56);
; #pragma unroll 1
;     for (int k = 120; k < 128; ++k) P11_V(k, cf_hi, vl, e_lo, k - 120);
	ds_read_b128 v[98:101], v4
	ds_read_b128 v[102:105], v4 offset:1024
	v_lshl_add_u64 v[2:3], v[72:73], 0, s[78:79]
	v_cvt_scalef32_pk_f32_fp4 v[136:137], v126, 1.0
	v_cvt_scalef32_pk_f32_fp4 v[138:139], v126, 1.0 op_sel:[1,0,0]
	v_cvt_scalef32_pk_f32_fp4 v[140:141], v126, 1.0 op_sel:[0,1,0]
	v_cvt_scalef32_pk_f32_fp4 v[142:143], v126, 1.0 op_sel:[1,1,0]
	v_pk_fma_f32 v[94:95], s[74:75], v[136:137], v[94:95] op_sel_hi:[0,1,1]
	v_pk_fma_f32 v[96:97], s[74:75], v[138:139], v[96:97] op_sel_hi:[0,1,1]
	v_pk_fma_f32 v[92:93], s[74:75], v[140:141], v[92:93] op_sel_hi:[0,1,1]
	v_pk_fma_f32 v[90:91], s[74:75], v[142:143], v[90:91] op_sel_hi:[0,1,1]
	v_cvt_scalef32_pk_f32_fp4 v[136:137], v127, 1.0
	v_cvt_scalef32_pk_f32_fp4 v[138:139], v127, 1.0 op_sel:[1,0,0]
	v_cvt_scalef32_pk_f32_fp4 v[140:141], v127, 1.0 op_sel:[0,1,0]
	v_cvt_scalef32_pk_f32_fp4 v[142:143], v127, 1.0 op_sel:[1,1,0]
	v_pk_fma_f32 v[88:89], s[74:75], v[136:137], v[88:89] op_sel_hi:[0,1,1]
	v_pk_fma_f32 v[86:87], s[74:75], v[138:139], v[86:87] op_sel_hi:[0,1,1]
	v_pk_fma_f32 v[84:85], s[74:75], v[140:141], v[84:85] op_sel_hi:[0,1,1]
	v_pk_fma_f32 v[82:83], s[74:75], v[142:143], v[82:83] op_sel_hi:[0,1,1]
	v_cvt_scalef32_pk_f32_fp4 v[136:137], v128, 1.0
	v_cvt_scalef32_pk_f32_fp4 v[138:139], v128, 1.0 op_sel:[1,0,0]
	v_cvt_scalef32_pk_f32_fp4 v[140:141], v128, 1.0 op_sel:[0,1,0]
	v_cvt_scalef32_pk_f32_fp4 v[142:143], v128, 1.0 op_sel:[1,1,0]
	v_pk_fma_f32 v[64:65], s[74:75], v[136:137], v[64:65] op_sel_hi:[0,1,1]
	v_pk_fma_f32 v[80:81], s[74:75], v[138:139], v[80:81] op_sel_hi:[0,1,1]
	v_pk_fma_f32 v[62:63], s[74:75], v[140:141], v[62:63] op_sel_hi:[0,1,1]
	v_pk_fma_f32 v[60:61], s[74:75], v[142:143], v[60:61] op_sel_hi:[0,1,1]
	s_waitcnt lgkmcnt(0)
	s_mov_b32 m0, s77
	s_nop 0
	global_load_lds_dwordx4 v[2:3], off
	global_load_lds_dwordx4 v[2:3], off offset:1024
	v_cvt_scalef32_pk_f32_fp4 v[136:137], v129, 1.0
	v_cvt_scalef32_pk_f32_fp4 v[138:139], v129, 1.0 op_sel:[1,0,0]
	v_cvt_scalef32_pk_f32_fp4 v[140:141], v129, 1.0 op_sel:[0,1,0]
	v_cvt_scalef32_pk_f32_fp4 v[142:143], v129, 1.0 op_sel:[1,1,0]
	v_pk_fma_f32 v[58:59], s[74:75], v[136:137], v[58:59] op_sel_hi:[0,1,1]
	v_pk_fma_f32 v[56:57], s[74:75], v[138:139], v[56:57] op_sel_hi:[0,1,1]
	v_pk_fma_f32 v[54:55], s[74:75], v[140:141], v[54:55] op_sel_hi:[0,1,1]
	v_pk_fma_f32 v[52:53], s[74:75], v[142:143], v[52:53] op_sel_hi:[0,1,1]
	v_cvt_scalef32_pk_f32_fp4 v[136:137], v130, 1.0
	v_cvt_scalef32_pk_f32_fp4 v[138:139], v130, 1.0 op_sel:[1,0,0]
	v_cvt_scalef32_pk_f32_fp4 v[140:141], v130, 1.0 op_sel:[0,1,0]
	v_cvt_scalef32_pk_f32_fp4 v[142:143], v130, 1.0 op_sel:[1,1,0]
	v_pk_fma_f32 v[50:51], s[74:75], v[136:137], v[50:51] op_sel_hi:[0,1,1]
	v_pk_fma_f32 v[48:49], s[74:75], v[138:139], v[48:49] op_sel_hi:[0,1,1]
	v_pk_fma_f32 v[46:47], s[74:75], v[140:141], v[46:47] op_sel_hi:[0,1,1]
	v_pk_fma_f32 v[44:45], s[74:75], v[142:143], v[44:45] op_sel_hi:[0,1,1]
	v_cvt_scalef32_pk_f32_fp4 v[136:137], v131, 1.0
	v_cvt_scalef32_pk_f32_fp4 v[138:139], v131, 1.0 op_sel:[1,0,0]
	v_cvt_scalef32_pk_f32_fp4 v[140:141], v131, 1.0 op_sel:[0,1,0]
	v_cvt_scalef32_pk_f32_fp4 v[142:143], v131, 1.0 op_sel:[1,1,0]
	v_pk_fma_f32 v[42:43], s[74:75], v[136:137], v[42:43] op_sel_hi:[0,1,1]
	v_pk_fma_f32 v[40:41], s[74:75], v[138:139], v[40:41] op_sel_hi:[0,1,1]
	v_pk_fma_f32 v[38:39], s[74:75], v[140:141], v[38:39] op_sel_hi:[0,1,1]
	v_pk_fma_f32 v[36:37], s[74:75], v[142:143], v[36:37] op_sel_hi:[0,1,1]
	v_cvt_scalef32_pk_f32_fp4 v[136:137], v132, 1.0
	v_cvt_scalef32_pk_f32_fp4 v[138:139], v132, 1.0 op_sel:[1,0,0]
	v_cvt_scalef32_pk_f32_fp4 v[140:141], v132, 1.0 op_sel:[0,1,0]
	v_cvt_scalef32_pk_f32_fp4 v[142:143], v132, 1.0 op_sel:[1,1,0]
	v_pk_fma_f32 v[32:33], s[74:75], v[136:137], v[32:33] op_sel_hi:[0,1,1]
	v_pk_fma_f32 v[34:35], s[74:75], v[138:139], v[34:35] op_sel_hi:[0,1,1]
	v_pk_fma_f32 v[30:31], s[74:75], v[140:141], v[30:31] op_sel_hi:[0,1,1]
	v_pk_fma_f32 v[28:29], s[74:75], v[142:143], v[28:29] op_sel_hi:[0,1,1]
	v_cvt_scalef32_pk_f32_fp4 v[136:137], v133, 1.0
	v_cvt_scalef32_pk_f32_fp4 v[138:139], v133, 1.0 op_sel:[1,0,0]
	v_cvt_scalef32_pk_f32_fp4 v[140:141], v133, 1.0 op_sel:[0,1,0]
	v_cvt_scalef32_pk_f32_fp4 v[142:143], v133, 1.0 op_sel:[1,1,0]
	v_pk_fma_f32 v[26:27], s[74:75], v[136:137], v[26:27] op_sel_hi:[0,1,1]
	v_pk_fma_f32 v[24:25], s[74:75], v[138:139], v[24:25] op_sel_hi:[0,1,1]
	v_pk_fma_f32 v[20:21], s[74:75], v[140:141], v[20:21] op_sel_hi:[0,1,1]
	v_pk_fma_f32 v[22:23], s[74:75], v[142:143], v[22:23] op_sel_hi:[0,1,1]
	s_add_i32 s46, s46, 2
	s_cmp_lg_u32 s46, 246
	s_cbranch_scc1 .Lv_sweep_hi
; DI void peer_token(LAS unsigned char* ring, const bf16* x1row, float inv2, const float* nffn, const int* ex, const float* pg, const unsigned char* U6, const unsigned char* V6,
;                    const float* usc, const float* vsc, float* orow, int lane) {
;     ...
;     for (int k = 64; k < 120; ++k) P11_V(k, cf_hi, vl, e_hi, k - 56);
; #pragma unroll 1
;     for (int k = 120; k < 128; ++k) P11_V(k, cf_hi, vl, e_lo, k - 120);
	s_add_i32 s47, s46, 1
	s_and_b32 s47, s47, 7
	s_lshl_b32 s47, s47, 11
	s_add_i32 s77, s33, s47
	v_add_u32_e32 v4, s77, v70
	s_add_i32 s78, s46, 9
	s_and_b32 s75, s78, 0x7f
	v_readlane_b32 s79, v113, s75
	v_readlane_b32 s47, v112, s75
	s_bitcmp1_b32 s75, 6
	s_cselect_b32 s47, s79, s47
	s_lshl_b32 s47, s47, 11
	s_bitcmp1_b32 s78, 7
	s_cselect_b32 s78, s98, 0
	s_cselect_b32 s79, s99, 0
	s_add_u32 s78, s78, s47
	s_addc_u32 s79, s79, 0
	v_readlane_b32 s74, v125, s46
	s_waitcnt vmcnt(14)
	ds_read_b128 v[126:129], v4
	ds_read_b128 v[130:133], v4 offset:1024
	v_lshl_add_u64 v[2:3], v[72:73], 0, s[78:79]
	v_cvt_scalef32_pk_f32_fp4 v[136:137], v98, 1.0
	v_cvt_scalef32_pk_f32_fp4 v[138:139], v98, 1.0 op_sel:[1,0,0]
	v_cvt_scalef32_pk_f32_fp4 v[140:141], v98, 1.0 op_sel:[0,1,0]
	v_cvt_scalef32_pk_f32_fp4 v[142:143], v98, 1.0 op_sel:[1,1,0]
	v_pk_fma_f32 v[94:95], s[74:75], v[136:137], v[94:95] op_sel_hi:[0,1,1]
	v_pk_fma_f32 v[96:97], s[74:75], v[138:139], v[96:97] op_sel_hi:[0,1,1]
	v_pk_fma_f32 v[92:93], s[74:75], v[140:141], v[92:93] op_sel_hi:[0,1,1]
	v_pk_fma_f32 v[90:91], s[74:75], v[142:143], v[90:91] op_sel_hi:[0,1,1]
	v_cvt_scalef32_pk_f32_fp4 v[136:137], v99, 1.0
	v_cvt_scalef32_pk_f32_fp4 v[138:139], v99, 1.0 op_sel:[1,0,0]
	v_cvt_scalef32_pk_f32_fp4 v[140:141], v99, 1.0 op_sel:[0,1,0]
	v_cvt_scalef32_pk_f32_fp4 v[142:143], v99, 1.0 op_sel:[1,1,0]
	v_pk_fma_f32 v[88:89], s[74:75], v[136:137], v[88:89] op_sel_hi:[0,1,1]
	v_pk_fma_f32 v[86:87], s[74:75], v[138:139], v[86:87] op_sel_hi:[0,1,1]
	v_pk_fma_f32 v[84:85], s[74:75], v[140:141], v[84:85] op_sel_hi:[0,1,1]
	v_pk_fma_f32 v[82:83], s[74:75], v[142:143], v[82:83] op_sel_hi:[0,1,1]
	v_cvt_scalef32_pk_f32_fp4 v[136:137], v100, 1.0
	v_cvt_scalef32_pk_f32_fp4 v[138:139], v100, 1.0 op_sel:[1,0,0]
	v_cvt_scalef32_pk_f32_fp4 v[140:141], v100, 1.0 op_sel:[0,1,0]
	v_cvt_scalef32_pk_f32_fp4 v[142:143], v100, 1.0 op_sel:[1,1,0]
	v_pk_fma_f32 v[64:65], s[74:75], v[136:137], v[64:65] op_sel_hi:[0,1,1]
	v_pk_fma_f32 v[80:81], s[74:75], v[138:139], v[80:81] op_sel_hi:[0,1,1]
	v_pk_fma_f32 v[62:63], s[74:75], v[140:141], v[62:63] op_sel_hi:[0,1,1]
	v_pk_fma_f32 v[60:61], s[74:75], v[142:143], v[60:61] op_sel_hi:[0,1,1]
	s_waitcnt lgkmcnt(0)
	s_mov_b32 m0, s77
	s_nop 0
	global_load_lds_dwordx4 v[2:3], off
	global_load_lds_dwordx4 v[2:3], off offset:1024
	v_cvt_scalef32_pk_f32_fp4 v[136:137], v101, 1.0
	v_cvt_scalef32_pk_f32_fp4 v[138:139], v101, 1.0 op_sel:[1,0,0]
	v_cvt_scalef32_pk_f32_fp4 v[140:141], v101, 1.0 op_sel:[0,1,0]
	v_cvt_scalef32_pk_f32_fp4 v[142:143], v101, 1.0 op_sel:[1,1,0]
	v_pk_fma_f32 v[58:59], s[74:75], v[136:137], v[58:59] op_sel_hi:[0,1,1]
	v_pk_fma_f32 v[56:57], s[74:75], v[138:139], v[56:57] op_sel_hi:[0,1,1]
	v_pk_fma_f32 v[54:55], s[74:75], v[140:141], v[54:55] op_sel_hi:[0,1,1]
	v_pk_fma_f32 v[52:53], s[74:75], v[142:143], v[52:53] op_sel_hi:[0,1,1]
	v_cvt_scalef32_pk_f32_fp4 v[136:137], v102, 1.0
	v_cvt_scalef32_pk_f32_fp4 v[138:139], v102, 1.0 op_sel:[1,0,0]
	v_cvt_scalef32_pk_f32_fp4 v[140:141], v102, 1.0 op_sel:[0,1,0]
	v_cvt_scalef32_pk_f32_fp4 v[142:143], v102, 1.0 op_sel:[1,1,0]
	v_pk_fma_f32 v[50:51], s[74:75], v[136:137], v[50:51] op_sel_hi:[0,1,1]
	v_pk_fma_f32 v[48:49], s[74:75], v[138:139], v[48:49] op_sel_hi:[0,1,1]
	v_pk_fma_f32 v[46:47], s[74:75], v[140:141], v[46:47] op_sel_hi:[0,1,1]
	v_pk_fma_f32 v[44:45], s[74:75], v[142:143], v[44:45] op_sel_hi:[0,1,1]
	v_cvt_scalef32_pk_f32_fp4 v[136:137], v103, 1.0
	v_cvt_scalef32_pk_f32_fp4 v[138:139], v103, 1.0 op_sel:[1,0,0]
	v_cvt_scalef32_pk_f32_fp4 v[140:141], v103, 1.0 op_sel:[0,1,0]
	v_cvt_scalef32_pk_f32_fp4 v[142:143], v103, 1.0 op_sel:[1,1,0]
	v_pk_fma_f32 v[42:43], s[74:75], v[136:137], v[42:43] op_sel_hi:[0,1,1]
	v_pk_fma_f32 v[40:41], s[74:75], v[138:139], v[40:41] op_sel_hi:[0,1,1]
	v_pk_fma_f32 v[38:39], s[74:75], v[140:141], v[38:39] op_sel_hi:[0,1,1]
	v_pk_fma_f32 v[36:37], s[74:75], v[142:143], v[36:37] op_sel_hi:[0,1,1]
	v_cvt_scalef32_pk_f32_fp4 v[136:137], v104, 1.0
	v_cvt_scalef32_pk_f32_fp4 v[138:139], v104, 1.0 op_sel:[1,0,0]
	v_cvt_scalef32_pk_f32_fp4 v[140:141], v104, 1.0 op_sel:[0,1,0]
	v_cvt_scalef32_pk_f32_fp4 v[142:143], v104, 1.0 op_sel:[1,1,0]
	v_pk_fma_f32 v[32:33], s[74:75], v[136:137], v[32:33] op_sel_hi:[0,1,1]
	v_pk_fma_f32 v[34:35], s[74:75], v[138:139], v[34:35] op_sel_hi:[0,1,1]
	v_pk_fma_f32 v[30:31], s[74:75], v[140:141], v[30:31] op_sel_hi:[0,1,1]
	v_pk_fma_f32 v[28:29], s[74:75], v[142:143], v[28:29] op_sel_hi:[0,1,1]
	v_cvt_scalef32_pk_f32_fp4 v[136:137], v105, 1.0
	v_cvt_scalef32_pk_f32_fp4 v[138:139], v105, 1.0 op_sel:[1,0,0]
	v_cvt_scalef32_pk_f32_fp4 v[140:141], v105, 1.0 op_sel:[0,1,0]
	v_cvt_scalef32_pk_f32_fp4 v[142:143], v105, 1.0 op_sel:[1,1,0]
	v_pk_fma_f32 v[26:27], s[74:75], v[136:137], v[26:27] op_sel_hi:[0,1,1]
	v_pk_fma_f32 v[24:25], s[74:75], v[138:139], v[24:25] op_sel_hi:[0,1,1]
	v_pk_fma_f32 v[20:21], s[74:75], v[140:141], v[20:21] op_sel_hi:[0,1,1]
	v_pk_fma_f32 v[22:23], s[74:75], v[142:143], v[22:23] op_sel_hi:[0,1,1]
	s_add_i32 s47, s46, 2
	s_and_b32 s47, s47, 7
	s_lshl_b32 s47, s47, 11
	s_add_i32 s77, s33, s47
	v_add_u32_e32 v4, s77, v70
	s_add_i32 s32, s46, 1
	v_readlane_b32 s74, v125, s32
	s_waitcnt vmcnt(14)
; DI void peer_token(LAS unsigned char* ring, const bf16* x1row, float inv2, const float* nffn, const int* ex, const float* pg, const unsigned char* U6, const unsigned char* V6,
;                    const float* usc, const float* vsc, float* orow, int lane) {
;     ...
;     for (int k = 64; k < 120; ++k) P11_V(k, cf_hi, vl, e_hi, k - 56);
; #pragma unroll 1
;     for (int k = 120; k < 128; ++k) P11_V(k, cf_hi, vl, e_lo, k - 120);
	ds_read_b128 v[98:101], v4
	ds_read_b128 v[102:105], v4 offset:1024
	v_cvt_scalef32_pk_f32_fp4 v[136:137], v126, 1.0
	v_cvt_scalef32_pk_f32_fp4 v[138:139], v126, 1.0 op_sel:[1,0,0]
	v_cvt_scalef32_pk_f32_fp4 v[140:141], v126, 1.0 op_sel:[0,1,0]
	v_cvt_scalef32_pk_f32_fp4 v[142:143], v126, 1.0 op_sel:[1,1,0]
	v_pk_fma_f32 v[94:95], s[74:75], v[136:137], v[94:95] op_sel_hi:[0,1,1]
	v_pk_fma_f32 v[96:97], s[74:75], v[138:139], v[96:97] op_sel_hi:[0,1,1]
	v_pk_fma_f32 v[92:93], s[74:75], v[140:141], v[92:93] op_sel_hi:[0,1,1]
	v_pk_fma_f32 v[90:91], s[74:75], v[142:143], v[90:91] op_sel_hi:[0,1,1]
	v_cvt_scalef32_pk_f32_fp4 v[136:137], v127, 1.0
	v_cvt_scalef32_pk_f32_fp4 v[138:139], v127, 1.0 op_sel:[1,0,0]
	v_cvt_scalef32_pk_f32_fp4 v[140:141], v127, 1.0 op_sel:[0,1,0]
	v_cvt_scalef32_pk_f32_fp4 v[142:143], v127, 1.0 op_sel:[1,1,0]
	v_pk_fma_f32 v[88:89], s[74:75], v[136:137], v[88:89] op_sel_hi:[0,1,1]
	v_pk_fma_f32 v[86:87], s[74:75], v[138:139], v[86:87] op_sel_hi:[0,1,1]
	v_pk_fma_f32 v[84:85], s[74:75], v[140:141], v[84:85] op_sel_hi:[0,1,1]
	v_pk_fma_f32 v[82:83], s[74:75], v[142:143], v[82:83] op_sel_hi:[0,1,1]
	v_cvt_scalef32_pk_f32_fp4 v[136:137], v128, 1.0
	v_cvt_scalef32_pk_f32_fp4 v[138:139], v128, 1.0 op_sel:[1,0,0]
	v_cvt_scalef32_pk_f32_fp4 v[140:141], v128, 1.0 op_sel:[0,1,0]
	v_cvt_scalef32_pk_f32_fp4 v[142:143], v128, 1.0 op_sel:[1,1,0]
	v_pk_fma_f32 v[64:65], s[74:75], v[136:137], v[64:65] op_sel_hi:[0,1,1]
	v_pk_fma_f32 v[80:81], s[74:75], v[138:139], v[80:81] op_sel_hi:[0,1,1]
	v_pk_fma_f32 v[62:63], s[74:75], v[140:141], v[62:63] op_sel_hi:[0,1,1]
	v_pk_fma_f32 v[60:61], s[74:75], v[142:143], v[60:61] op_sel_hi:[0,1,1]
	s_waitcnt lgkmcnt(0)
	v_cvt_scalef32_pk_f32_fp4 v[136:137], v129, 1.0
	v_cvt_scalef32_pk_f32_fp4 v[138:139], v129, 1.0 op_sel:[1,0,0]
	v_cvt_scalef32_pk_f32_fp4 v[140:141], v129, 1.0 op_sel:[0,1,0]
	v_cvt_scalef32_pk_f32_fp4 v[142:143], v129, 1.0 op_sel:[1,1,0]
	v_pk_fma_f32 v[58:59], s[74:75], v[136:137], v[58:59] op_sel_hi:[0,1,1]
	v_pk_fma_f32 v[56:57], s[74:75], v[138:139], v[56:57] op_sel_hi:[0,1,1]
	v_pk_fma_f32 v[54:55], s[74:75], v[140:141], v[54:55] op_sel_hi:[0,1,1]
	v_pk_fma_f32 v[52:53], s[74:75], v[142:143], v[52:53] op_sel_hi:[0,1,1]
	v_cvt_scalef32_pk_f32_fp4 v[136:137], v130, 1.0
	v_cvt_scalef32_pk_f32_fp4 v[138:139], v130, 1.0 op_sel:[1,0,0]
	v_cvt_scalef32_pk_f32_fp4 v[140:141], v130, 1.0 op_sel:[0,1,0]
	v_cvt_scalef32_pk_f32_fp4 v[142:143], v130, 1.0 op_sel:[1,1,0]
	v_pk_fma_f32 v[50:51], s[74:75], v[136:137], v[50:51] op_sel_hi:[0,1,1]
	v_pk_fma_f32 v[48:49], s[74:75], v[138:139], v[48:49] op_sel_hi:[0,1,1]
	v_pk_fma_f32 v[46:47], s[74:75], v[140:141], v[46:47] op_sel_hi:[0,1,1]
	v_pk_fma_f32 v[44:45], s[74:75], v[142:143], v[44:45] op_sel_hi:[0,1,1]
	v_cvt_scalef32_pk_f32_fp4 v[136:137], v131, 1.0
	v_cvt_scalef32_pk_f32_fp4 v[138:139], v131, 1.0 op_sel:[1,0,0]
	v_cvt_scalef32_pk_f32_fp4 v[140:141], v131, 1.0 op_sel:[0,1,0]
	v_cvt_scalef32_pk_f32_fp4 v[142:143], v131, 1.0 op_sel:[1,1,0]
	v_pk_fma_f32 v[42:43], s[74:75], v[136:137], v[42:43] op_sel_hi:[0,1,1]
	v_pk_fma_f32 v[40:41], s[74:75], v[138:139], v[40:41] op_sel_hi:[0,1,1]
	v_pk_fma_f32 v[38:39], s[74:75], v[140:141], v[38:39] op_sel_hi:[0,1,1]
	v_pk_fma_f32 v[36:37], s[74:75], v[142:143], v[36:37] op_sel_hi:[0,1,1]
	v_cvt_scalef32_pk_f32_fp4 v[136:137], v132, 1.0
	v_cvt_scalef32_pk_f32_fp4 v[138:139], v132, 1.0 op_sel:[1,0,0]
	v_cvt_scalef32_pk_f32_fp4 v[140:141], v132, 1.0 op_sel:[0,1,0]
	v_cvt_scalef32_pk_f32_fp4 v[142:143], v132, 1.0 op_sel:[1,1,0]
	v_pk_fma_f32 v[32:33], s[74:75], v[136:137], v[32:33] op_sel_hi:[0,1,1]
	v_pk_fma_f32 v[34:35], s[74:75], v[138:139], v[34:35] op_sel_hi:[0,1,1]
	v_pk_fma_f32 v[30:31], s[74:75], v[140:141], v[30:31] op_sel_hi:[0,1,1]
	v_pk_fma_f32 v[28:29], s[74:75], v[142:143], v[28:29] op_sel_hi:[0,1,1]
	v_cvt_scalef32_pk_f32_fp4 v[136:137], v133, 1.0
	v_cvt_scalef32_pk_f32_fp4 v[138:139], v133, 1.0 op_sel:[1,0,0]
	v_cvt_scalef32_pk_f32_fp4 v[140:141], v133, 1.0 op_sel:[0,1,0]
	v_cvt_scalef32_pk_f32_fp4 v[142:143], v133, 1.0 op_sel:[1,1,0]
	v_pk_fma_f32 v[26:27], s[74:75], v[136:137], v[26:27] op_sel_hi:[0,1,1]
	v_pk_fma_f32 v[24:25], s[74:75], v[138:139], v[24:25] op_sel_hi:[0,1,1]
	v_pk_fma_f32 v[20:21], s[74:75], v[140:141], v[20:21] op_sel_hi:[0,1,1]
	v_pk_fma_f32 v[22:23], s[74:75], v[142:143], v[22:23] op_sel_hi:[0,1,1]
	s_add_i32 s47, s46, 3
	s_and_b32 s47, s47, 7
	s_lshl_b32 s47, s47, 11
	s_add_i32 s77, s33, s47
	v_add_u32_e32 v4, s77, v70
	s_add_i32 s32, s46, 2
	v_readlane_b32 s74, v125, s32
	s_waitcnt vmcnt(12)
	ds_read_b128 v[126:129], v4
	ds_read_b128 v[130:133], v4 offset:1024
	v_cvt_scalef32_pk_f32_fp4 v[136:137], v98, 1.0
	v_cvt_scalef32_pk_f32_fp4 v[138:139], v98, 1.0 op_sel:[1,0,0]
	v_cvt_scalef32_pk_f32_fp4 v[140:141], v98, 1.0 op_sel:[0,1,0]
	v_cvt_scalef32_pk_f32_fp4 v[142:143], v98, 1.0 op_sel:[1,1,0]
	v_pk_fma_f32 v[94:95], s[74:75], v[136:137], v[94:95] op_sel_hi:[0,1,1]
	v_pk_fma_f32 v[96:97], s[74:75], v[138:139], v[96:97] op_sel_hi:[0,1,1]
	v_pk_fma_f32 v[92:93], s[74:75], v[140:141], v[92:93] op_sel_hi:[0,1,1]
	v_pk_fma_f32 v[90:91], s[74:75], v[142:143], v[90:91] op_sel_hi:[0,1,1]
	v_cvt_scalef32_pk_f32_fp4 v[136:137], v99, 1.0
	v_cvt_scalef32_pk_f32_fp4 v[138:139], v99, 1.0 op_sel:[1,0,0]
	v_cvt_scalef32_pk_f32_fp4 v[140:141], v99, 1.0 op_sel:[0,1,0]
	v_cvt_scalef32_pk_f32_fp4 v[142:143], v99, 1.0 op_sel:[1,1,0]
	v_pk_fma_f32 v[88:89], s[74:75], v[136:137], v[88:89] op_sel_hi:[0,1,1]
	v_pk_fma_f32 v[86:87], s[74:75], v[138:139], v[86:87] op_sel_hi:[0,1,1]
	v_pk_fma_f32 v[84:85], s[74:75], v[140:141], v[84:85] op_sel_hi:[0,1,1]
	v_pk_fma_f32 v[82:83], s[74:75], v[142:143], v[82:83] op_sel_hi:[0,1,1]
	v_cvt_scalef32_pk_f32_fp4 v[136:137], v100, 1.0
	v_cvt_scalef32_pk_f32_fp4 v[138:139], v100, 1.0 op_sel:[1,0,0]
	v_cvt_scalef32_pk_f32_fp4 v[140:141], v100, 1.0 op_sel:[0,1,0]
	v_cvt_scalef32_pk_f32_fp4 v[142:143], v100, 1.0 op_sel:[1,1,0]
	v_pk_fma_f32 v[64:65], s[74:75], v[136:137], v[64:65] op_sel_hi:[0,1,1]
	v_pk_fma_f32 v[80:81], s[74:75], v[138:139], v[80:81] op_sel_hi:[0,1,1]
	v_pk_fma_f32 v[62:63], s[74:75], v[140:141], v[62:63] op_sel_hi:[0,1,1]
	v_pk_fma_f32 v[60:61], s[74:75], v[142:143], v[60:61] op_sel_hi:[0,1,1]
	s_waitcnt lgkmcnt(0)
; DI void peer_token(LAS unsigned char* ring, const bf16* x1row, float inv2, const float* nffn, const int* ex, const float* pg, const unsigned char* U6, const unsigned char* V6,
;                    const float* usc, const float* vsc, float* orow, int lane) {
;     ...
;     for (int k = 64; k < 120; ++k) P11_V(k, cf_hi, vl, e_hi, k - 56);
; #pragma unroll 1
;     for (int k = 120; k < 128; ++k) P11_V(k, cf_hi, vl, e_lo, k - 120);
	v_cvt_scalef32_pk_f32_fp4 v[136:137], v101, 1.0
	v_cvt_scalef32_pk_f32_fp4 v[138:139], v101, 1.0 op_sel:[1,0,0]
	v_cvt_scalef32_pk_f32_fp4 v[140:141], v101, 1.0 op_sel:[0,1,0]
	v_cvt_scalef32_pk_f32_fp4 v[142:143], v101, 1.0 op_sel:[1,1,0]
	v_pk_fma_f32 v[58:59], s[74:75], v[136:137], v[58:59] op_sel_hi:[0,1,1]
	v_pk_fma_f32 v[56:57], s[74:75], v[138:139], v[56:57] op_sel_hi:[0,1,1]
	v_pk_fma_f32 v[54:55], s[74:75], v[140:141], v[54:55] op_sel_hi:[0,1,1]
	v_pk_fma_f32 v[52:53], s[74:75], v[142:143], v[52:53] op_sel_hi:[0,1,1]
	v_cvt_scalef32_pk_f32_fp4 v[136:137], v102, 1.0
	v_cvt_scalef32_pk_f32_fp4 v[138:139], v102, 1.0 op_sel:[1,0,0]
	v_cvt_scalef32_pk_f32_fp4 v[140:141], v102, 1.0 op_sel:[0,1,0]
	v_cvt_scalef32_pk_f32_fp4 v[142:143], v102, 1.0 op_sel:[1,1,0]
	v_pk_fma_f32 v[50:51], s[74:75], v[136:137], v[50:51] op_sel_hi:[0,1,1]
	v_pk_fma_f32 v[48:49], s[74:75], v[138:139], v[48:49] op_sel_hi:[0,1,1]
	v_pk_fma_f32 v[46:47], s[74:75], v[140:141], v[46:47] op_sel_hi:[0,1,1]
	v_pk_fma_f32 v[44:45], s[74:75], v[142:143], v[44:45] op_sel_hi:[0,1,1]
	v_cvt_scalef32_pk_f32_fp4 v[136:137], v103, 1.0
	v_cvt_scalef32_pk_f32_fp4 v[138:139], v103, 1.0 op_sel:[1,0,0]
	v_cvt_scalef32_pk_f32_fp4 v[140:141], v103, 1.0 op_sel:[0,1,0]
	v_cvt_scalef32_pk_f32_fp4 v[142:143], v103, 1.0 op_sel:[1,1,0]
	v_pk_fma_f32 v[42:43], s[74:75], v[136:137], v[42:43] op_sel_hi:[0,1,1]
	v_pk_fma_f32 v[40:41], s[74:75], v[138:139], v[40:41] op_sel_hi:[0,1,1]
	v_pk_fma_f32 v[38:39], s[74:75], v[140:141], v[38:39] op_sel_hi:[0,1,1]
	v_pk_fma_f32 v[36:37], s[74:75], v[142:143], v[36:37] op_sel_hi:[0,1,1]
	v_cvt_scalef32_pk_f32_fp4 v[136:137], v104, 1.0
	v_cvt_scalef32_pk_f32_fp4 v[138:139], v104, 1.0 op_sel:[1,0,0]
	v_cvt_scalef32_pk_f32_fp4 v[140:141], v104, 1.0 op_sel:[0,1,0]
	v_cvt_scalef32_pk_f32_fp4 v[142:143], v104, 1.0 op_sel:[1,1,0]
	v_pk_fma_f32 v[32:33], s[74:75], v[136:137], v[32:33] op_sel_hi:[0,1,1]
	v_pk_fma_f32 v[34:35], s[74:75], v[138:139], v[34:35] op_sel_hi:[0,1,1]
	v_pk_fma_f32 v[30:31], s[74:75], v[140:141], v[30:31] op_sel_hi:[0,1,1]
	v_pk_fma_f32 v[28:29], s[74:75], v[142:143], v[28:29] op_sel_hi:[0,1,1]
	v_cvt_scalef32_pk_f32_fp4 v[136:137], v105, 1.0
	v_cvt_scalef32_pk_f32_fp4 v[138:139], v105, 1.0 op_sel:[1,0,0]
	v_cvt_scalef32_pk_f32_fp4 v[140:141], v105, 1.0 op_sel:[0,1,0]
	v_cvt_scalef32_pk_f32_fp4 v[142:143], v105, 1.0 op_sel:[1,1,0]
	v_pk_fma_f32 v[26:27], s[74:75], v[136:137], v[26:27] op_sel_hi:[0,1,1]
	v_pk_fma_f32 v[24:25], s[74:75], v[138:139], v[24:25] op_sel_hi:[0,1,1]
	v_pk_fma_f32 v[20:21], s[74:75], v[140:141], v[20:21] op_sel_hi:[0,1,1]
	v_pk_fma_f32 v[22:23], s[74:75], v[142:143], v[22:23] op_sel_hi:[0,1,1]
	s_add_i32 s47, s46, 4
	s_and_b32 s47, s47, 7
	s_lshl_b32 s47, s47, 11
	s_add_i32 s77, s33, s47
	v_add_u32_e32 v4, s77, v70
	s_add_i32 s32, s46, 3
	v_readlane_b32 s74, v125, s32
	s_waitcnt vmcnt(10)
	ds_read_b128 v[98:101], v4
	ds_read_b128 v[102:105], v4 offset:1024
	v_cvt_scalef32_pk_f32_fp4 v[136:137], v126, 1.0
	v_cvt_scalef32_pk_f32_fp4 v[138:139], v126, 1.0 op_sel:[1,0,0]
	v_cvt_scalef32_pk_f32_fp4 v[140:141], v126, 1.0 op_sel:[0,1,0]
	v_cvt_scalef32_pk_f32_fp4 v[142:143], v126, 1.0 op_sel:[1,1,0]
	v_pk_fma_f32 v[94:95], s[74:75], v[136:137], v[94:95] op_sel_hi:[0,1,1]
	v_pk_fma_f32 v[96:97], s[74:75], v[138:139], v[96:97] op_sel_hi:[0,1,1]
	v_pk_fma_f32 v[92:93], s[74:75], v[140:141], v[92:93] op_sel_hi:[0,1,1]
	v_pk_fma_f32 v[90:91], s[74:75], v[142:143], v[90:91] op_sel_hi:[0,1,1]
	v_cvt_scalef32_pk_f32_fp4 v[136:137], v127, 1.0
	v_cvt_scalef32_pk_f32_fp4 v[138:139], v127, 1.0 op_sel:[1,0,0]
	v_cvt_scalef32_pk_f32_fp4 v[140:141], v127, 1.0 op_sel:[0,1,0]
	v_cvt_scalef32_pk_f32_fp4 v[142:143], v127, 1.0 op_sel:[1,1,0]
	v_pk_fma_f32 v[88:89], s[74:75], v[136:137], v[88:89] op_sel_hi:[0,1,1]
	v_pk_fma_f32 v[86:87], s[74:75], v[138:139], v[86:87] op_sel_hi:[0,1,1]
	v_pk_fma_f32 v[84:85], s[74:75], v[140:141], v[84:85] op_sel_hi:[0,1,1]
	v_pk_fma_f32 v[82:83], s[74:75], v[142:143], v[82:83] op_sel_hi:[0,1,1]
	v_cvt_scalef32_pk_f32_fp4 v[136:137], v128, 1.0
	v_cvt_scalef32_pk_f32_fp4 v[138:139], v128, 1.0 op_sel:[1,0,0]
	v_cvt_scalef32_pk_f32_fp4 v[140:141], v128, 1.0 op_sel:[0,1,0]
	v_cvt_scalef32_pk_f32_fp4 v[142:143], v128, 1.0 op_sel:[1,1,0]
	v_pk_fma_f32 v[64:65], s[74:75], v[136:137], v[64:65] op_sel_hi:[0,1,1]
	v_pk_fma_f32 v[80:81], s[74:75], v[138:139], v[80:81] op_sel_hi:[0,1,1]
	v_pk_fma_f32 v[62:63], s[74:75], v[140:141], v[62:63] op_sel_hi:[0,1,1]
	v_pk_fma_f32 v[60:61], s[74:75], v[142:143], v[60:61] op_sel_hi:[0,1,1]
	s_waitcnt lgkmcnt(0)
	v_cvt_scalef32_pk_f32_fp4 v[136:137], v129, 1.0
	v_cvt_scalef32_pk_f32_fp4 v[138:139], v129, 1.0 op_sel:[1,0,0]
	v_cvt_scalef32_pk_f32_fp4 v[140:141], v129, 1.0 op_sel:[0,1,0]
	v_cvt_scalef32_pk_f32_fp4 v[142:143], v129, 1.0 op_sel:[1,1,0]
	v_pk_fma_f32 v[58:59], s[74:75], v[136:137], v[58:59] op_sel_hi:[0,1,1]
	v_pk_fma_f32 v[56:57], s[74:75], v[138:139], v[56:57] op_sel_hi:[0,1,1]
	v_pk_fma_f32 v[54:55], s[74:75], v[140:141], v[54:55] op_sel_hi:[0,1,1]
	v_pk_fma_f32 v[52:53], s[74:75], v[142:143], v[52:53] op_sel_hi:[0,1,1]
	v_cvt_scalef32_pk_f32_fp4 v[136:137], v130, 1.0
	v_cvt_scalef32_pk_f32_fp4 v[138:139], v130, 1.0 op_sel:[1,0,0]
	v_cvt_scalef32_pk_f32_fp4 v[140:141], v130, 1.0 op_sel:[0,1,0]
	v_cvt_scalef32_pk_f32_fp4 v[142:143], v130, 1.0 op_sel:[1,1,0]
	v_pk_fma_f32 v[50:51], s[74:75], v[136:137], v[50:51] op_sel_hi:[0,1,1]
	v_pk_fma_f32 v[48:49], s[74:75], v[138:139], v[48:49] op_sel_hi:[0,1,1]
	v_pk_fma_f32 v[46:47], s[74:75], v[140:141], v[46:47] op_sel_hi:[0,1,1]
	v_pk_fma_f32 v[44:45], s[74:75], v[142:143], v[44:45] op_sel_hi:[0,1,1]
	v_cvt_scalef32_pk_f32_fp4 v[136:137], v131, 1.0
	v_cvt_scalef32_pk_f32_fp4 v[138:139], v131, 1.0 op_sel:[1,0,0]
	v_cvt_scalef32_pk_f32_fp4 v[140:141], v131, 1.0 op_sel:[0,1,0]
	v_cvt_scalef32_pk_f32_fp4 v[142:143], v131, 1.0 op_sel:[1,1,0]
	v_pk_fma_f32 v[42:43], s[74:75], v[136:137], v[42:43] op_sel_hi:[0,1,1]
	v_pk_fma_f32 v[40:41], s[74:75], v[138:139], v[40:41] op_sel_hi:[0,1,1]
	v_pk_fma_f32 v[38:39], s[74:75], v[140:141], v[38:39] op_sel_hi:[0,1,1]
	v_pk_fma_f32 v[36:37], s[74:75], v[142:143], v[36:37] op_sel_hi:[0,1,1]
	v_cvt_scalef32_pk_f32_fp4 v[136:137], v132, 1.0
	v_cvt_scalef32_pk_f32_fp4 v[138:139], v132, 1.0 op_sel:[1,0,0]
	v_cvt_scalef32_pk_f32_fp4 v[140:141], v132, 1.0 op_sel:[0,1,0]
	v_cvt_scalef32_pk_f32_fp4 v[142:143], v132, 1.0 op_sel:[1,1,0]
	v_pk_fma_f32 v[32:33], s[74:75], v[136:137], v[32:33] op_sel_hi:[0,1,1]
	v_pk_fma_f32 v[34:35], s[74:75], v[138:139], v[34:35] op_sel_hi:[0,1,1]
	v_pk_fma_f32 v[30:31], s[74:75], v[140:141], v[30:31] op_sel_hi:[0,1,1]
	v_pk_fma_f32 v[28:29], s[74:75], v[142:143], v[28:29] op_sel_hi:[0,1,1]
	v_cvt_scalef32_pk_f32_fp4 v[136:137], v133, 1.0
	v_cvt_scalef32_pk_f32_fp4 v[138:139], v133, 1.0 op_sel:[1,0,0]
	v_cvt_scalef32_pk_f32_fp4 v[140:141], v133, 1.0 op_sel:[0,1,0]
	v_cvt_scalef32_pk_f32_fp4 v[142:143], v133, 1.0 op_sel:[1,1,0]
	v_pk_fma_f32 v[26:27], s[74:75], v[136:137], v[26:27] op_sel_hi:[0,1,1]
	v_pk_fma_f32 v[24:25], s[74:75], v[138:139], v[24:25] op_sel_hi:[0,1,1]
	v_pk_fma_f32 v[20:21], s[74:75], v[140:141], v[20:21] op_sel_hi:[0,1,1]
	v_pk_fma_f32 v[22:23], s[74:75], v[142:143], v[22:23] op_sel_hi:[0,1,1]
	s_add_i32 s47, s46, 5
	s_and_b32 s47, s47, 7
	s_lshl_b32 s47, s47, 11
	s_add_i32 s77, s33, s47
	v_add_u32_e32 v4, s77, v70
	s_add_i32 s32, s46, 4
	v_readlane_b32 s74, v125, s32
	s_waitcnt vmcnt(8)
	ds_read_b128 v[126:129], v4
	ds_read_b128 v[130:133], v4 offset:1024
	v_cvt_scalef32_pk_f32_fp4 v[136:137], v98, 1.0
	v_cvt_scalef32_pk_f32_fp4 v[138:139], v98, 1.0 op_sel:[1,0,0]
	v_cvt_scalef32_pk_f32_fp4 v[140:141], v98, 1.0 op_sel:[0,1,0]
	v_cvt_scalef32_pk_f32_fp4 v[142:143], v98, 1.0 op_sel:[1,1,0]
	v_pk_fma_f32 v[94:95], s[74:75], v[136:137], v[94:95] op_sel_hi:[0,1,1]
	v_pk_fma_f32 v[96:97], s[74:75], v[138:139], v[96:97] op_sel_hi:[0,1,1]
	v_pk_fma_f32 v[92:93], s[74:75], v[140:141], v[92:93] op_sel_hi:[0,1,1]
	v_pk_fma_f32 v[90:91], s[74:75], v[142:143], v[90:91] op_sel_hi:[0,1,1]
	v_cvt_scalef32_pk_f32_fp4 v[136:137], v99, 1.0
	v_cvt_scalef32_pk_f32_fp4 v[138:139], v99, 1.0 op_sel:[1,0,0]
	v_cvt_scalef32_pk_f32_fp4 v[140:141], v99, 1.0 op_sel:[0,1,0]
	v_cvt_scalef32_pk_f32_fp4 v[142:143], v99, 1.0 op_sel:[1,1,0]
	v_pk_fma_f32 v[88:89], s[74:75], v[136:137], v[88:89] op_sel_hi:[0,1,1]
	v_pk_fma_f32 v[86:87], s[74:75], v[138:139], v[86:87] op_sel_hi:[0,1,1]
	v_pk_fma_f32 v[84:85], s[74:75], v[140:141], v[84:85] op_sel_hi:[0,1,1]
	v_pk_fma_f32 v[82:83], s[74:75], v[142:143], v[82:83] op_sel_hi:[0,1,1]
	v_cvt_scalef32_pk_f32_fp4 v[136:137], v100, 1.0
	v_cvt_scalef32_pk_f32_fp4 v[138:139], v100, 1.0 op_sel:[1,0,0]
	v_cvt_scalef32_pk_f32_fp4 v[140:141], v100, 1.0 op_sel:[0,1,0]
	v_cvt_scalef32_pk_f32_fp4 v[142:143], v100, 1.0 op_sel:[1,1,0]
	v_pk_fma_f32 v[64:65], s[74:75], v[136:137], v[64:65] op_sel_hi:[0,1,1]
	v_pk_fma_f32 v[80:81], s[74:75], v[138:139], v[80:81] op_sel_hi:[0,1,1]
	v_pk_fma_f32 v[62:63], s[74:75], v[140:141], v[62:63] op_sel_hi:[0,1,1]
	v_pk_fma_f32 v[60:61], s[74:75], v[142:143], v[60:61] op_sel_hi:[0,1,1]
	s_waitcnt lgkmcnt(0)
	v_cvt_scalef32_pk_f32_fp4 v[136:137], v101, 1.0
	v_cvt_scalef32_pk_f32_fp4 v[138:139], v101, 1.0 op_sel:[1,0,0]
	v_cvt_scalef32_pk_f32_fp4 v[140:141], v101, 1.0 op_sel:[0,1,0]
	v_cvt_scalef32_pk_f32_fp4 v[142:143], v101, 1.0 op_sel:[1,1,0]
	v_pk_fma_f32 v[58:59], s[74:75], v[136:137], v[58:59] op_sel_hi:[0,1,1]
	v_pk_fma_f32 v[56:57], s[74:75], v[138:139], v[56:57] op_sel_hi:[0,1,1]
	v_pk_fma_f32 v[54:55], s[74:75], v[140:141], v[54:55] op_sel_hi:[0,1,1]
	v_pk_fma_f32 v[52:53], s[74:75], v[142:143], v[52:53] op_sel_hi:[0,1,1]
	v_cvt_scalef32_pk_f32_fp4 v[136:137], v102, 1.0
	v_cvt_scalef32_pk_f32_fp4 v[138:139], v102, 1.0 op_sel:[1,0,0]
	v_cvt_scalef32_pk_f32_fp4 v[140:141], v102, 1.0 op_sel:[0,1,0]
	v_cvt_scalef32_pk_f32_fp4 v[142:143], v102, 1.0 op_sel:[1,1,0]
	v_pk_fma_f32 v[50:51], s[74:75], v[136:137], v[50:51] op_sel_hi:[0,1,1]
	v_pk_fma_f32 v[48:49], s[74:75], v[138:139], v[48:49] op_sel_hi:[0,1,1]
	v_pk_fma_f32 v[46:47], s[74:75], v[140:141], v[46:47] op_sel_hi:[0,1,1]
	v_pk_fma_f32 v[44:45], s[74:75], v[142:143], v[44:45] op_sel_hi:[0,1,1]
	v_cvt_scalef32_pk_f32_fp4 v[136:137], v103, 1.0
	v_cvt_scalef32_pk_f32_fp4 v[138:139], v103, 1.0 op_sel:[1,0,0]
	v_cvt_scalef32_pk_f32_fp4 v[140:141], v103, 1.0 op_sel:[0,1,0]
	v_cvt_scalef32_pk_f32_fp4 v[142:143], v103, 1.0 op_sel:[1,1,0]
	v_pk_fma_f32 v[42:43], s[74:75], v[136:137], v[42:43] op_sel_hi:[0,1,1]
	v_pk_fma_f32 v[40:41], s[74:75], v[138:139], v[40:41] op_sel_hi:[0,1,1]
	v_pk_fma_f32 v[38:39], s[74:75], v[140:141], v[38:39] op_sel_hi:[0,1,1]
	v_pk_fma_f32 v[36:37], s[74:75], v[142:143], v[36:37] op_sel_hi:[0,1,1]
	v_cvt_scalef32_pk_f32_fp4 v[136:137], v104, 1.0
	v_cvt_scalef32_pk_f32_fp4 v[138:139], v104, 1.0 op_sel:[1,0,0]
	v_cvt_scalef32_pk_f32_fp4 v[140:141], v104, 1.0 op_sel:[0,1,0]
	v_cvt_scalef32_pk_f32_fp4 v[142:143], v104, 1.0 op_sel:[1,1,0]
	v_pk_fma_f32 v[32:33], s[74:75], v[136:137], v[32:33] op_sel_hi:[0,1,1]
	v_pk_fma_f32 v[34:35], s[74:75], v[138:139], v[34:35] op_sel_hi:[0,1,1]
	v_pk_fma_f32 v[30:31], s[74:75], v[140:141], v[30:31] op_sel_hi:[0,1,1]
	v_pk_fma_f32 v[28:29], s[74:75], v[142:143], v[28:29] op_sel_hi:[0,1,1]
	v_cvt_scalef32_pk_f32_fp4 v[136:137], v105, 1.0
	v_cvt_scalef32_pk_f32_fp4 v[138:139], v105, 1.0 op_sel:[1,0,0]
	v_cvt_scalef32_pk_f32_fp4 v[140:141], v105, 1.0 op_sel:[0,1,0]
	v_cvt_scalef32_pk_f32_fp4 v[142:143], v105, 1.0 op_sel:[1,1,0]
	v_pk_fma_f32 v[26:27], s[74:75], v[136:137], v[26:27] op_sel_hi:[0,1,1]
	v_pk_fma_f32 v[24:25], s[74:75], v[138:139], v[24:25] op_sel_hi:[0,1,1]
	v_pk_fma_f32 v[20:21], s[74:75], v[140:141], v[20:21] op_sel_hi:[0,1,1]
	v_pk_fma_f32 v[22:23], s[74:75], v[142:143], v[22:23] op_sel_hi:[0,1,1]
	s_add_i32 s47, s46, 6
	s_and_b32 s47, s47, 7
	s_lshl_b32 s47, s47, 11
	s_add_i32 s77, s33, s47
	v_add_u32_e32 v4, s77, v70
	s_add_i32 s32, s46, 5
	v_readlane_b32 s74, v125, s32
	s_waitcnt vmcnt(6)
	ds_read_b128 v[98:101], v4
	ds_read_b128 v[102:105], v4 offset:1024
	v_cvt_scalef32_pk_f32_fp4 v[136:137], v126, 1.0
	v_cvt_scalef32_pk_f32_fp4 v[138:139], v126, 1.0 op_sel:[1,0,0]
	v_cvt_scalef32_pk_f32_fp4 v[140:141], v126, 1.0 op_sel:[0,1,0]
	v_cvt_scalef32_pk_f32_fp4 v[142:143], v126, 1.0 op_sel:[1,1,0]
	v_pk_fma_f32 v[94:95], s[74:75], v[136:137], v[94:95] op_sel_hi:[0,1,1]
	v_pk_fma_f32 v[96:97], s[74:75], v[138:139], v[96:97] op_sel_hi:[0,1,1]
	v_pk_fma_f32 v[92:93], s[74:75], v[140:141], v[92:93] op_sel_hi:[0,1,1]
	v_pk_fma_f32 v[90:91], s[74:75], v[142:143], v[90:91] op_sel_hi:[0,1,1]
	v_cvt_scalef32_pk_f32_fp4 v[136:137], v127, 1.0
	v_cvt_scalef32_pk_f32_fp4 v[138:139], v127, 1.0 op_sel:[1,0,0]
	v_cvt_scalef32_pk_f32_fp4 v[140:141], v127, 1.0 op_sel:[0,1,0]
	v_cvt_scalef32_pk_f32_fp4 v[142:143], v127, 1.0 op_sel:[1,1,0]
	v_pk_fma_f32 v[88:89], s[74:75], v[136:137], v[88:89] op_sel_hi:[0,1,1]
	v_pk_fma_f32 v[86:87], s[74:75], v[138:139], v[86:87] op_sel_hi:[0,1,1]
	v_pk_fma_f32 v[84:85], s[74:75], v[140:141], v[84:85] op_sel_hi:[0,1,1]
	v_pk_fma_f32 v[82:83], s[74:75], v[142:143], v[82:83] op_sel_hi:[0,1,1]
	v_cvt_scalef32_pk_f32_fp4 v[136:137], v128, 1.0
	v_cvt_scalef32_pk_f32_fp4 v[138:139], v128, 1.0 op_sel:[1,0,0]
	v_cvt_scalef32_pk_f32_fp4 v[140:141], v128, 1.0 op_sel:[0,1,0]
	v_cvt_scalef32_pk_f32_fp4 v[142:143], v128, 1.0 op_sel:[1,1,0]
	v_pk_fma_f32 v[64:65], s[74:75], v[136:137], v[64:65] op_sel_hi:[0,1,1]
	v_pk_fma_f32 v[80:81], s[74:75], v[138:139], v[80:81] op_sel_hi:[0,1,1]
	v_pk_fma_f32 v[62:63], s[74:75], v[140:141], v[62:63] op_sel_hi:[0,1,1]
	v_pk_fma_f32 v[60:61], s[74:75], v[142:143], v[60:61] op_sel_hi:[0,1,1]
	s_waitcnt lgkmcnt(0)
	v_cvt_scalef32_pk_f32_fp4 v[136:137], v129, 1.0
	v_cvt_scalef32_pk_f32_fp4 v[138:139], v129, 1.0 op_sel:[1,0,0]
	v_cvt_scalef32_pk_f32_fp4 v[140:141], v129, 1.0 op_sel:[0,1,0]
	v_cvt_scalef32_pk_f32_fp4 v[142:143], v129, 1.0 op_sel:[1,1,0]
	v_pk_fma_f32 v[58:59], s[74:75], v[136:137], v[58:59] op_sel_hi:[0,1,1]
	v_pk_fma_f32 v[56:57], s[74:75], v[138:139], v[56:57] op_sel_hi:[0,1,1]
	v_pk_fma_f32 v[54:55], s[74:75], v[140:141], v[54:55] op_sel_hi:[0,1,1]
	v_pk_fma_f32 v[52:53], s[74:75], v[142:143], v[52:53] op_sel_hi:[0,1,1]
	v_cvt_scalef32_pk_f32_fp4 v[136:137], v130, 1.0
	v_cvt_scalef32_pk_f32_fp4 v[138:139], v130, 1.0 op_sel:[1,0,0]
	v_cvt_scalef32_pk_f32_fp4 v[140:141], v130, 1.0 op_sel:[0,1,0]
	v_cvt_scalef32_pk_f32_fp4 v[142:143], v130, 1.0 op_sel:[1,1,0]
	v_pk_fma_f32 v[50:51], s[74:75], v[136:137], v[50:51] op_sel_hi:[0,1,1]
	v_pk_fma_f32 v[48:49], s[74:75], v[138:139], v[48:49] op_sel_hi:[0,1,1]
	v_pk_fma_f32 v[46:47], s[74:75], v[140:141], v[46:47] op_sel_hi:[0,1,1]
	v_pk_fma_f32 v[44:45], s[74:75], v[142:143], v[44:45] op_sel_hi:[0,1,1]
	v_cvt_scalef32_pk_f32_fp4 v[136:137], v131, 1.0
	v_cvt_scalef32_pk_f32_fp4 v[138:139], v131, 1.0 op_sel:[1,0,0]
	v_cvt_scalef32_pk_f32_fp4 v[140:141], v131, 1.0 op_sel:[0,1,0]
	v_cvt_scalef32_pk_f32_fp4 v[142:143], v131, 1.0 op_sel:[1,1,0]
	v_pk_fma_f32 v[42:43], s[74:75], v[136:137], v[42:43] op_sel_hi:[0,1,1]
	v_pk_fma_f32 v[40:41], s[74:75], v[138:139], v[40:41] op_sel_hi:[0,1,1]
	v_pk_fma_f32 v[38:39], s[74:75], v[140:141], v[38:39] op_sel_hi:[0,1,1]
	v_pk_fma_f32 v[36:37], s[74:75], v[142:143], v[36:37] op_sel_hi:[0,1,1]
	v_cvt_scalef32_pk_f32_fp4 v[136:137], v132, 1.0
	v_cvt_scalef32_pk_f32_fp4 v[138:139], v132, 1.0 op_sel:[1,0,0]
	v_cvt_scalef32_pk_f32_fp4 v[140:141], v132, 1.0 op_sel:[0,1,0]
	v_cvt_scalef32_pk_f32_fp4 v[142:143], v132, 1.0 op_sel:[1,1,0]
	v_pk_fma_f32 v[32:33], s[74:75], v[136:137], v[32:33] op_sel_hi:[0,1,1]
	v_pk_fma_f32 v[34:35], s[74:75], v[138:139], v[34:35] op_sel_hi:[0,1,1]
	v_pk_fma_f32 v[30:31], s[74:75], v[140:141], v[30:31] op_sel_hi:[0,1,1]
	v_pk_fma_f32 v[28:29], s[74:75], v[142:143], v[28:29] op_sel_hi:[0,1,1]
	v_cvt_scalef32_pk_f32_fp4 v[136:137], v133, 1.0
	v_cvt_scalef32_pk_f32_fp4 v[138:139], v133, 1.0 op_sel:[1,0,0]
	v_cvt_scalef32_pk_f32_fp4 v[140:141], v133, 1.0 op_sel:[0,1,0]
	v_cvt_scalef32_pk_f32_fp4 v[142:143], v133, 1.0 op_sel:[1,1,0]
	v_pk_fma_f32 v[26:27], s[74:75], v[136:137], v[26:27] op_sel_hi:[0,1,1]
	v_pk_fma_f32 v[24:25], s[74:75], v[138:139], v[24:25] op_sel_hi:[0,1,1]
	v_pk_fma_f32 v[20:21], s[74:75], v[140:141], v[20:21] op_sel_hi:[0,1,1]
	v_pk_fma_f32 v[22:23], s[74:75], v[142:143], v[22:23] op_sel_hi:[0,1,1]
	s_add_i32 s47, s46, 7
	s_and_b32 s47, s47, 7
	s_lshl_b32 s47, s47, 11
	s_add_i32 s77, s33, s47
	v_add_u32_e32 v4, s77, v70
	s_add_i32 s32, s46, 6
	v_readlane_b32 s74, v125, s32
	s_waitcnt vmcnt(4)
	ds_read_b128 v[126:129], v4
	ds_read_b128 v[130:133], v4 offset:1024
	v_cvt_scalef32_pk_f32_fp4 v[136:137], v98, 1.0
	v_cvt_scalef32_pk_f32_fp4 v[138:139], v98, 1.0 op_sel:[1,0,0]
	v_cvt_scalef32_pk_f32_fp4 v[140:141], v98, 1.0 op_sel:[0,1,0]
	v_cvt_scalef32_pk_f32_fp4 v[142:143], v98, 1.0 op_sel:[1,1,0]
	v_pk_fma_f32 v[94:95], s[74:75], v[136:137], v[94:95] op_sel_hi:[0,1,1]
	v_pk_fma_f32 v[96:97], s[74:75], v[138:139], v[96:97] op_sel_hi:[0,1,1]
	v_pk_fma_f32 v[92:93], s[74:75], v[140:141], v[92:93] op_sel_hi:[0,1,1]
	v_pk_fma_f32 v[90:91], s[74:75], v[142:143], v[90:91] op_sel_hi:[0,1,1]
	v_cvt_scalef32_pk_f32_fp4 v[136:137], v99, 1.0
	v_cvt_scalef32_pk_f32_fp4 v[138:139], v99, 1.0 op_sel:[1,0,0]
	v_cvt_scalef32_pk_f32_fp4 v[140:141], v99, 1.0 op_sel:[0,1,0]
	v_cvt_scalef32_pk_f32_fp4 v[142:143], v99, 1.0 op_sel:[1,1,0]
	v_pk_fma_f32 v[88:89], s[74:75], v[136:137], v[88:89] op_sel_hi:[0,1,1]
	v_pk_fma_f32 v[86:87], s[74:75], v[138:139], v[86:87] op_sel_hi:[0,1,1]
	v_pk_fma_f32 v[84:85], s[74:75], v[140:141], v[84:85] op_sel_hi:[0,1,1]
	v_pk_fma_f32 v[82:83], s[74:75], v[142:143], v[82:83] op_sel_hi:[0,1,1]
	v_cvt_scalef32_pk_f32_fp4 v[136:137], v100, 1.0
	v_cvt_scalef32_pk_f32_fp4 v[138:139], v100, 1.0 op_sel:[1,0,0]
	v_cvt_scalef32_pk_f32_fp4 v[140:141], v100, 1.0 op_sel:[0,1,0]
	v_cvt_scalef32_pk_f32_fp4 v[142:143], v100, 1.0 op_sel:[1,1,0]
	v_pk_fma_f32 v[64:65], s[74:75], v[136:137], v[64:65] op_sel_hi:[0,1,1]
	v_pk_fma_f32 v[80:81], s[74:75], v[138:139], v[80:81] op_sel_hi:[0,1,1]
	v_pk_fma_f32 v[62:63], s[74:75], v[140:141], v[62:63] op_sel_hi:[0,1,1]
	v_pk_fma_f32 v[60:61], s[74:75], v[142:143], v[60:61] op_sel_hi:[0,1,1]
	s_waitcnt lgkmcnt(0)
	v_cvt_scalef32_pk_f32_fp4 v[136:137], v101, 1.0
	v_cvt_scalef32_pk_f32_fp4 v[138:139], v101, 1.0 op_sel:[1,0,0]
	v_cvt_scalef32_pk_f32_fp4 v[140:141], v101, 1.0 op_sel:[0,1,0]
	v_cvt_scalef32_pk_f32_fp4 v[142:143], v101, 1.0 op_sel:[1,1,0]
	v_pk_fma_f32 v[58:59], s[74:75], v[136:137], v[58:59] op_sel_hi:[0,1,1]
	v_pk_fma_f32 v[56:57], s[74:75], v[138:139], v[56:57] op_sel_hi:[0,1,1]
	v_pk_fma_f32 v[54:55], s[74:75], v[140:141], v[54:55] op_sel_hi:[0,1,1]
	v_pk_fma_f32 v[52:53], s[74:75], v[142:143], v[52:53] op_sel_hi:[0,1,1]
	v_cvt_scalef32_pk_f32_fp4 v[136:137], v102, 1.0
	v_cvt_scalef32_pk_f32_fp4 v[138:139], v102, 1.0 op_sel:[1,0,0]
	v_cvt_scalef32_pk_f32_fp4 v[140:141], v102, 1.0 op_sel:[0,1,0]
	v_cvt_scalef32_pk_f32_fp4 v[142:143], v102, 1.0 op_sel:[1,1,0]
	v_pk_fma_f32 v[50:51], s[74:75], v[136:137], v[50:51] op_sel_hi:[0,1,1]
	v_pk_fma_f32 v[48:49], s[74:75], v[138:139], v[48:49] op_sel_hi:[0,1,1]
	v_pk_fma_f32 v[46:47], s[74:75], v[140:141], v[46:47] op_sel_hi:[0,1,1]
	v_pk_fma_f32 v[44:45], s[74:75], v[142:143], v[44:45] op_sel_hi:[0,1,1]
	v_cvt_scalef32_pk_f32_fp4 v[136:137], v103, 1.0
	v_cvt_scalef32_pk_f32_fp4 v[138:139], v103, 1.0 op_sel:[1,0,0]
	v_cvt_scalef32_pk_f32_fp4 v[140:141], v103, 1.0 op_sel:[0,1,0]
	v_cvt_scalef32_pk_f32_fp4 v[142:143], v103, 1.0 op_sel:[1,1,0]
	v_pk_fma_f32 v[42:43], s[74:75], v[136:137], v[42:43] op_sel_hi:[0,1,1]
	v_pk_fma_f32 v[40:41], s[74:75], v[138:139], v[40:41] op_sel_hi:[0,1,1]
	v_pk_fma_f32 v[38:39], s[74:75], v[140:141], v[38:39] op_sel_hi:[0,1,1]
	v_pk_fma_f32 v[36:37], s[74:75], v[142:143], v[36:37] op_sel_hi:[0,1,1]
	v_cvt_scalef32_pk_f32_fp4 v[136:137], v104, 1.0
	v_cvt_scalef32_pk_f32_fp4 v[138:139], v104, 1.0 op_sel:[1,0,0]
	v_cvt_scalef32_pk_f32_fp4 v[140:141], v104, 1.0 op_sel:[0,1,0]
	v_cvt_scalef32_pk_f32_fp4 v[142:143], v104, 1.0 op_sel:[1,1,0]
	v_pk_fma_f32 v[32:33], s[74:75], v[136:137], v[32:33] op_sel_hi:[0,1,1]
	v_pk_fma_f32 v[34:35], s[74:75], v[138:139], v[34:35] op_sel_hi:[0,1,1]
	v_pk_fma_f32 v[30:31], s[74:75], v[140:141], v[30:31] op_sel_hi:[0,1,1]
	v_pk_fma_f32 v[28:29], s[74:75], v[142:143], v[28:29] op_sel_hi:[0,1,1]
	v_cvt_scalef32_pk_f32_fp4 v[136:137], v105, 1.0
	v_cvt_scalef32_pk_f32_fp4 v[138:139], v105, 1.0 op_sel:[1,0,0]
	v_cvt_scalef32_pk_f32_fp4 v[140:141], v105, 1.0 op_sel:[0,1,0]
	v_cvt_scalef32_pk_f32_fp4 v[142:143], v105, 1.0 op_sel:[1,1,0]
	v_pk_fma_f32 v[26:27], s[74:75], v[136:137], v[26:27] op_sel_hi:[0,1,1]
	v_pk_fma_f32 v[24:25], s[74:75], v[138:139], v[24:25] op_sel_hi:[0,1,1]
	v_pk_fma_f32 v[20:21], s[74:75], v[140:141], v[20:21] op_sel_hi:[0,1,1]
	v_pk_fma_f32 v[22:23], s[74:75], v[142:143], v[22:23] op_sel_hi:[0,1,1]
	s_add_i32 s47, s46, 8
	s_and_b32 s47, s47, 7
	s_lshl_b32 s47, s47, 11
	s_add_i32 s77, s33, s47
	v_add_u32_e32 v4, s77, v70
	s_add_i32 s32, s46, 7
	v_readlane_b32 s74, v125, s32
	s_waitcnt vmcnt(2)
	ds_read_b128 v[98:101], v4
	ds_read_b128 v[102:105], v4 offset:1024
	v_cvt_scalef32_pk_f32_fp4 v[136:137], v126, 1.0
	v_cvt_scalef32_pk_f32_fp4 v[138:139], v126, 1.0 op_sel:[1,0,0]
	v_cvt_scalef32_pk_f32_fp4 v[140:141], v126, 1.0 op_sel:[0,1,0]
	v_cvt_scalef32_pk_f32_fp4 v[142:143], v126, 1.0 op_sel:[1,1,0]
	v_pk_fma_f32 v[94:95], s[74:75], v[136:137], v[94:95] op_sel_hi:[0,1,1]
	v_pk_fma_f32 v[96:97], s[74:75], v[138:139], v[96:97] op_sel_hi:[0,1,1]
	v_pk_fma_f32 v[92:93], s[74:75], v[140:141], v[92:93] op_sel_hi:[0,1,1]
	v_pk_fma_f32 v[90:91], s[74:75], v[142:143], v[90:91] op_sel_hi:[0,1,1]
	v_cvt_scalef32_pk_f32_fp4 v[136:137], v127, 1.0
	v_cvt_scalef32_pk_f32_fp4 v[138:139], v127, 1.0 op_sel:[1,0,0]
	v_cvt_scalef32_pk_f32_fp4 v[140:141], v127, 1.0 op_sel:[0,1,0]
	v_cvt_scalef32_pk_f32_fp4 v[142:143], v127, 1.0 op_sel:[1,1,0]
	v_pk_fma_f32 v[88:89], s[74:75], v[136:137], v[88:89] op_sel_hi:[0,1,1]
	v_pk_fma_f32 v[86:87], s[74:75], v[138:139], v[86:87] op_sel_hi:[0,1,1]
	v_pk_fma_f32 v[84:85], s[74:75], v[140:141], v[84:85] op_sel_hi:[0,1,1]
	v_pk_fma_f32 v[82:83], s[74:75], v[142:143], v[82:83] op_sel_hi:[0,1,1]
	v_cvt_scalef32_pk_f32_fp4 v[136:137], v128, 1.0
	v_cvt_scalef32_pk_f32_fp4 v[138:139], v128, 1.0 op_sel:[1,0,0]
	v_cvt_scalef32_pk_f32_fp4 v[140:141], v128, 1.0 op_sel:[0,1,0]
	v_cvt_scalef32_pk_f32_fp4 v[142:143], v128, 1.0 op_sel:[1,1,0]
	v_pk_fma_f32 v[64:65], s[74:75], v[136:137], v[64:65] op_sel_hi:[0,1,1]
	v_pk_fma_f32 v[80:81], s[74:75], v[138:139], v[80:81] op_sel_hi:[0,1,1]
	v_pk_fma_f32 v[62:63], s[74:75], v[140:141], v[62:63] op_sel_hi:[0,1,1]
	v_pk_fma_f32 v[60:61], s[74:75], v[142:143], v[60:61] op_sel_hi:[0,1,1]
	s_waitcnt lgkmcnt(0)
	v_cvt_scalef32_pk_f32_fp4 v[136:137], v129, 1.0
	v_cvt_scalef32_pk_f32_fp4 v[138:139], v129, 1.0 op_sel:[1,0,0]
	v_cvt_scalef32_pk_f32_fp4 v[140:141], v129, 1.0 op_sel:[0,1,0]
	v_cvt_scalef32_pk_f32_fp4 v[142:143], v129, 1.0 op_sel:[1,1,0]
	v_pk_fma_f32 v[58:59], s[74:75], v[136:137], v[58:59] op_sel_hi:[0,1,1]
	v_pk_fma_f32 v[56:57], s[74:75], v[138:139], v[56:57] op_sel_hi:[0,1,1]
	v_pk_fma_f32 v[54:55], s[74:75], v[140:141], v[54:55] op_sel_hi:[0,1,1]
	v_pk_fma_f32 v[52:53], s[74:75], v[142:143], v[52:53] op_sel_hi:[0,1,1]
	v_cvt_scalef32_pk_f32_fp4 v[136:137], v130, 1.0
	v_cvt_scalef32_pk_f32_fp4 v[138:139], v130, 1.0 op_sel:[1,0,0]
	v_cvt_scalef32_pk_f32_fp4 v[140:141], v130, 1.0 op_sel:[0,1,0]
	v_cvt_scalef32_pk_f32_fp4 v[142:143], v130, 1.0 op_sel:[1,1,0]
	v_pk_fma_f32 v[50:51], s[74:75], v[136:137], v[50:51] op_sel_hi:[0,1,1]
	v_pk_fma_f32 v[48:49], s[74:75], v[138:139], v[48:49] op_sel_hi:[0,1,1]
	v_pk_fma_f32 v[46:47], s[74:75], v[140:141], v[46:47] op_sel_hi:[0,1,1]
	v_pk_fma_f32 v[44:45], s[74:75], v[142:143], v[44:45] op_sel_hi:[0,1,1]
	v_cvt_scalef32_pk_f32_fp4 v[136:137], v131, 1.0
	v_cvt_scalef32_pk_f32_fp4 v[138:139], v131, 1.0 op_sel:[1,0,0]
	v_cvt_scalef32_pk_f32_fp4 v[140:141], v131, 1.0 op_sel:[0,1,0]
	v_cvt_scalef32_pk_f32_fp4 v[142:143], v131, 1.0 op_sel:[1,1,0]
	v_pk_fma_f32 v[42:43], s[74:75], v[136:137], v[42:43] op_sel_hi:[0,1,1]
	v_pk_fma_f32 v[40:41], s[74:75], v[138:139], v[40:41] op_sel_hi:[0,1,1]
	v_pk_fma_f32 v[38:39], s[74:75], v[140:141], v[38:39] op_sel_hi:[0,1,1]
	v_pk_fma_f32 v[36:37], s[74:75], v[142:143], v[36:37] op_sel_hi:[0,1,1]
	v_cvt_scalef32_pk_f32_fp4 v[136:137], v132, 1.0
	v_cvt_scalef32_pk_f32_fp4 v[138:139], v132, 1.0 op_sel:[1,0,0]
	v_cvt_scalef32_pk_f32_fp4 v[140:141], v132, 1.0 op_sel:[0,1,0]
	v_cvt_scalef32_pk_f32_fp4 v[142:143], v132, 1.0 op_sel:[1,1,0]
	v_pk_fma_f32 v[32:33], s[74:75], v[136:137], v[32:33] op_sel_hi:[0,1,1]
	v_pk_fma_f32 v[34:35], s[74:75], v[138:139], v[34:35] op_sel_hi:[0,1,1]
	v_pk_fma_f32 v[30:31], s[74:75], v[140:141], v[30:31] op_sel_hi:[0,1,1]
	v_pk_fma_f32 v[28:29], s[74:75], v[142:143], v[28:29] op_sel_hi:[0,1,1]
	v_cvt_scalef32_pk_f32_fp4 v[136:137], v133, 1.0
	v_cvt_scalef32_pk_f32_fp4 v[138:139], v133, 1.0 op_sel:[1,0,0]
	v_cvt_scalef32_pk_f32_fp4 v[140:141], v133, 1.0 op_sel:[0,1,0]
	v_cvt_scalef32_pk_f32_fp4 v[142:143], v133, 1.0 op_sel:[1,1,0]
	v_pk_fma_f32 v[26:27], s[74:75], v[136:137], v[26:27] op_sel_hi:[0,1,1]
	v_pk_fma_f32 v[24:25], s[74:75], v[138:139], v[24:25] op_sel_hi:[0,1,1]
	v_pk_fma_f32 v[20:21], s[74:75], v[140:141], v[20:21] op_sel_hi:[0,1,1]
	v_pk_fma_f32 v[22:23], s[74:75], v[142:143], v[22:23] op_sel_hi:[0,1,1]
	s_add_i32 s47, s46, 9
	s_and_b32 s47, s47, 7
	s_lshl_b32 s47, s47, 11
	s_add_i32 s77, s33, s47
	v_add_u32_e32 v4, s77, v70
	s_add_i32 s32, s46, 8
	v_readlane_b32 s74, v125, s32
	s_waitcnt vmcnt(0)
	ds_read_b128 v[126:129], v4
	ds_read_b128 v[130:133], v4 offset:1024
	v_cvt_scalef32_pk_f32_fp4 v[136:137], v98, 1.0
	v_cvt_scalef32_pk_f32_fp4 v[138:139], v98, 1.0 op_sel:[1,0,0]
	v_cvt_scalef32_pk_f32_fp4 v[140:141], v98, 1.0 op_sel:[0,1,0]
	v_cvt_scalef32_pk_f32_fp4 v[142:143], v98, 1.0 op_sel:[1,1,0]
	v_pk_fma_f32 v[94:95], s[74:75], v[136:137], v[94:95] op_sel_hi:[0,1,1]
	v_pk_fma_f32 v[96:97], s[74:75], v[138:139], v[96:97] op_sel_hi:[0,1,1]
	v_pk_fma_f32 v[92:93], s[74:75], v[140:141], v[92:93] op_sel_hi:[0,1,1]
	v_pk_fma_f32 v[90:91], s[74:75], v[142:143], v[90:91] op_sel_hi:[0,1,1]
	v_cvt_scalef32_pk_f32_fp4 v[136:137], v99, 1.0
	v_cvt_scalef32_pk_f32_fp4 v[138:139], v99, 1.0 op_sel:[1,0,0]
	v_cvt_scalef32_pk_f32_fp4 v[140:141], v99, 1.0 op_sel:[0,1,0]
	v_cvt_scalef32_pk_f32_fp4 v[142:143], v99, 1.0 op_sel:[1,1,0]
	v_pk_fma_f32 v[88:89], s[74:75], v[136:137], v[88:89] op_sel_hi:[0,1,1]
	v_pk_fma_f32 v[86:87], s[74:75], v[138:139], v[86:87] op_sel_hi:[0,1,1]
	v_pk_fma_f32 v[84:85], s[74:75], v[140:141], v[84:85] op_sel_hi:[0,1,1]
	v_pk_fma_f32 v[82:83], s[74:75], v[142:143], v[82:83] op_sel_hi:[0,1,1]
	v_cvt_scalef32_pk_f32_fp4 v[136:137], v100, 1.0
	v_cvt_scalef32_pk_f32_fp4 v[138:139], v100, 1.0 op_sel:[1,0,0]
	v_cvt_scalef32_pk_f32_fp4 v[140:141], v100, 1.0 op_sel:[0,1,0]
	v_cvt_scalef32_pk_f32_fp4 v[142:143], v100, 1.0 op_sel:[1,1,0]
	v_pk_fma_f32 v[64:65], s[74:75], v[136:137], v[64:65] op_sel_hi:[0,1,1]
	v_pk_fma_f32 v[80:81], s[74:75], v[138:139], v[80:81] op_sel_hi:[0,1,1]
	v_pk_fma_f32 v[62:63], s[74:75], v[140:141], v[62:63] op_sel_hi:[0,1,1]
	v_pk_fma_f32 v[60:61], s[74:75], v[142:143], v[60:61] op_sel_hi:[0,1,1]
	s_waitcnt lgkmcnt(0)
; DI void peer_token(LAS unsigned char* ring, const bf16* x1row, float inv2, const float* nffn, const int* ex, const float* pg, const unsigned char* U6, const unsigned char* V6,
;                    const float* usc, const float* vsc, float* orow, int lane) {
;     ...
;     asm volatile("s_waitcnt vmcnt(0)" ::: "memory");
	v_cvt_scalef32_pk_f32_fp4 v[136:137], v101, 1.0
	v_cvt_scalef32_pk_f32_fp4 v[138:139], v101, 1.0 op_sel:[1,0,0]
	v_cvt_scalef32_pk_f32_fp4 v[140:141], v101, 1.0 op_sel:[0,1,0]
	v_cvt_scalef32_pk_f32_fp4 v[142:143], v101, 1.0 op_sel:[1,1,0]
	v_pk_fma_f32 v[58:59], s[74:75], v[136:137], v[58:59] op_sel_hi:[0,1,1]
	v_pk_fma_f32 v[56:57], s[74:75], v[138:139], v[56:57] op_sel_hi:[0,1,1]
	v_pk_fma_f32 v[54:55], s[74:75], v[140:141], v[54:55] op_sel_hi:[0,1,1]
	v_pk_fma_f32 v[52:53], s[74:75], v[142:143], v[52:53] op_sel_hi:[0,1,1]
	v_cvt_scalef32_pk_f32_fp4 v[136:137], v102, 1.0
	v_cvt_scalef32_pk_f32_fp4 v[138:139], v102, 1.0 op_sel:[1,0,0]
	v_cvt_scalef32_pk_f32_fp4 v[140:141], v102, 1.0 op_sel:[0,1,0]
	v_cvt_scalef32_pk_f32_fp4 v[142:143], v102, 1.0 op_sel:[1,1,0]
	v_pk_fma_f32 v[50:51], s[74:75], v[136:137], v[50:51] op_sel_hi:[0,1,1]
	v_pk_fma_f32 v[48:49], s[74:75], v[138:139], v[48:49] op_sel_hi:[0,1,1]
	v_pk_fma_f32 v[46:47], s[74:75], v[140:141], v[46:47] op_sel_hi:[0,1,1]
	v_pk_fma_f32 v[44:45], s[74:75], v[142:143], v[44:45] op_sel_hi:[0,1,1]
	v_cvt_scalef32_pk_f32_fp4 v[136:137], v103, 1.0
	v_cvt_scalef32_pk_f32_fp4 v[138:139], v103, 1.0 op_sel:[1,0,0]
	v_cvt_scalef32_pk_f32_fp4 v[140:141], v103, 1.0 op_sel:[0,1,0]
	v_cvt_scalef32_pk_f32_fp4 v[142:143], v103, 1.0 op_sel:[1,1,0]
	v_pk_fma_f32 v[42:43], s[74:75], v[136:137], v[42:43] op_sel_hi:[0,1,1]
	v_pk_fma_f32 v[40:41], s[74:75], v[138:139], v[40:41] op_sel_hi:[0,1,1]
	v_pk_fma_f32 v[38:39], s[74:75], v[140:141], v[38:39] op_sel_hi:[0,1,1]
	v_pk_fma_f32 v[36:37], s[74:75], v[142:143], v[36:37] op_sel_hi:[0,1,1]
	v_cvt_scalef32_pk_f32_fp4 v[136:137], v104, 1.0
	v_cvt_scalef32_pk_f32_fp4 v[138:139], v104, 1.0 op_sel:[1,0,0]
	v_cvt_scalef32_pk_f32_fp4 v[140:141], v104, 1.0 op_sel:[0,1,0]
	v_cvt_scalef32_pk_f32_fp4 v[142:143], v104, 1.0 op_sel:[1,1,0]
	v_pk_fma_f32 v[32:33], s[74:75], v[136:137], v[32:33] op_sel_hi:[0,1,1]
	v_pk_fma_f32 v[34:35], s[74:75], v[138:139], v[34:35] op_sel_hi:[0,1,1]
	v_pk_fma_f32 v[30:31], s[74:75], v[140:141], v[30:31] op_sel_hi:[0,1,1]
	v_pk_fma_f32 v[28:29], s[74:75], v[142:143], v[28:29] op_sel_hi:[0,1,1]
	v_cvt_scalef32_pk_f32_fp4 v[136:137], v105, 1.0
	v_cvt_scalef32_pk_f32_fp4 v[138:139], v105, 1.0 op_sel:[1,0,0]
	v_cvt_scalef32_pk_f32_fp4 v[140:141], v105, 1.0 op_sel:[0,1,0]
	v_cvt_scalef32_pk_f32_fp4 v[142:143], v105, 1.0 op_sel:[1,1,0]
	v_pk_fma_f32 v[26:27], s[74:75], v[136:137], v[26:27] op_sel_hi:[0,1,1]
	v_pk_fma_f32 v[24:25], s[74:75], v[138:139], v[24:25] op_sel_hi:[0,1,1]
	v_pk_fma_f32 v[20:21], s[74:75], v[140:141], v[20:21] op_sel_hi:[0,1,1]
	v_pk_fma_f32 v[22:23], s[74:75], v[142:143], v[22:23] op_sel_hi:[0,1,1]
	s_add_i32 s32, s46, 9
	v_readlane_b32 s74, v125, s32
	s_nop 1
	v_cvt_scalef32_pk_f32_fp4 v[136:137], v126, 1.0
	v_cvt_scalef32_pk_f32_fp4 v[138:139], v126, 1.0 op_sel:[1,0,0]
	v_cvt_scalef32_pk_f32_fp4 v[140:141], v126, 1.0 op_sel:[0,1,0]
	v_cvt_scalef32_pk_f32_fp4 v[142:143], v126, 1.0 op_sel:[1,1,0]
	v_pk_fma_f32 v[94:95], s[74:75], v[136:137], v[94:95] op_sel_hi:[0,1,1]
	v_pk_fma_f32 v[96:97], s[74:75], v[138:139], v[96:97] op_sel_hi:[0,1,1]
	v_pk_fma_f32 v[92:93], s[74:75], v[140:141], v[92:93] op_sel_hi:[0,1,1]
	v_pk_fma_f32 v[90:91], s[74:75], v[142:143], v[90:91] op_sel_hi:[0,1,1]
	v_cvt_scalef32_pk_f32_fp4 v[136:137], v127, 1.0
	v_cvt_scalef32_pk_f32_fp4 v[138:139], v127, 1.0 op_sel:[1,0,0]
	v_cvt_scalef32_pk_f32_fp4 v[140:141], v127, 1.0 op_sel:[0,1,0]
	v_cvt_scalef32_pk_f32_fp4 v[142:143], v127, 1.0 op_sel:[1,1,0]
	v_pk_fma_f32 v[88:89], s[74:75], v[136:137], v[88:89] op_sel_hi:[0,1,1]
	v_pk_fma_f32 v[86:87], s[74:75], v[138:139], v[86:87] op_sel_hi:[0,1,1]
	v_pk_fma_f32 v[84:85], s[74:75], v[140:141], v[84:85] op_sel_hi:[0,1,1]
	v_pk_fma_f32 v[82:83], s[74:75], v[142:143], v[82:83] op_sel_hi:[0,1,1]
	v_cvt_scalef32_pk_f32_fp4 v[136:137], v128, 1.0
	v_cvt_scalef32_pk_f32_fp4 v[138:139], v128, 1.0 op_sel:[1,0,0]
	v_cvt_scalef32_pk_f32_fp4 v[140:141], v128, 1.0 op_sel:[0,1,0]
	v_cvt_scalef32_pk_f32_fp4 v[142:143], v128, 1.0 op_sel:[1,1,0]
	v_pk_fma_f32 v[64:65], s[74:75], v[136:137], v[64:65] op_sel_hi:[0,1,1]
	v_pk_fma_f32 v[80:81], s[74:75], v[138:139], v[80:81] op_sel_hi:[0,1,1]
	v_pk_fma_f32 v[62:63], s[74:75], v[140:141], v[62:63] op_sel_hi:[0,1,1]
	v_pk_fma_f32 v[60:61], s[74:75], v[142:143], v[60:61] op_sel_hi:[0,1,1]
	v_cvt_scalef32_pk_f32_fp4 v[136:137], v129, 1.0
	v_cvt_scalef32_pk_f32_fp4 v[138:139], v129, 1.0 op_sel:[1,0,0]
	v_cvt_scalef32_pk_f32_fp4 v[140:141], v129, 1.0 op_sel:[0,1,0]
	v_cvt_scalef32_pk_f32_fp4 v[142:143], v129, 1.0 op_sel:[1,1,0]
	v_pk_fma_f32 v[58:59], s[74:75], v[136:137], v[58:59] op_sel_hi:[0,1,1]
	v_pk_fma_f32 v[56:57], s[74:75], v[138:139], v[56:57] op_sel_hi:[0,1,1]
	v_pk_fma_f32 v[54:55], s[74:75], v[140:141], v[54:55] op_sel_hi:[0,1,1]
	v_pk_fma_f32 v[52:53], s[74:75], v[142:143], v[52:53] op_sel_hi:[0,1,1]
	v_cvt_scalef32_pk_f32_fp4 v[136:137], v130, 1.0
	v_cvt_scalef32_pk_f32_fp4 v[138:139], v130, 1.0 op_sel:[1,0,0]
	v_cvt_scalef32_pk_f32_fp4 v[140:141], v130, 1.0 op_sel:[0,1,0]
	v_cvt_scalef32_pk_f32_fp4 v[142:143], v130, 1.0 op_sel:[1,1,0]
	v_pk_fma_f32 v[50:51], s[74:75], v[136:137], v[50:51] op_sel_hi:[0,1,1]
	v_pk_fma_f32 v[48:49], s[74:75], v[138:139], v[48:49] op_sel_hi:[0,1,1]
	v_pk_fma_f32 v[46:47], s[74:75], v[140:141], v[46:47] op_sel_hi:[0,1,1]
	v_pk_fma_f32 v[44:45], s[74:75], v[142:143], v[44:45] op_sel_hi:[0,1,1]
	v_cvt_scalef32_pk_f32_fp4 v[136:137], v131, 1.0
	v_cvt_scalef32_pk_f32_fp4 v[138:139], v131, 1.0 op_sel:[1,0,0]
	v_cvt_scalef32_pk_f32_fp4 v[140:141], v131, 1.0 op_sel:[0,1,0]
	v_cvt_scalef32_pk_f32_fp4 v[142:143], v131, 1.0 op_sel:[1,1,0]
	v_pk_fma_f32 v[42:43], s[74:75], v[136:137], v[42:43] op_sel_hi:[0,1,1]
	v_pk_fma_f32 v[40:41], s[74:75], v[138:139], v[40:41] op_sel_hi:[0,1,1]
	v_pk_fma_f32 v[38:39], s[74:75], v[140:141], v[38:39] op_sel_hi:[0,1,1]
	v_pk_fma_f32 v[36:37], s[74:75], v[142:143], v[36:37] op_sel_hi:[0,1,1]
	v_cvt_scalef32_pk_f32_fp4 v[136:137], v132, 1.0
	v_cvt_scalef32_pk_f32_fp4 v[138:139], v132, 1.0 op_sel:[1,0,0]
	v_cvt_scalef32_pk_f32_fp4 v[140:141], v132, 1.0 op_sel:[0,1,0]
	v_cvt_scalef32_pk_f32_fp4 v[142:143], v132, 1.0 op_sel:[1,1,0]
	v_pk_fma_f32 v[32:33], s[74:75], v[136:137], v[32:33] op_sel_hi:[0,1,1]
	v_pk_fma_f32 v[34:35], s[74:75], v[138:139], v[34:35] op_sel_hi:[0,1,1]
	v_pk_fma_f32 v[30:31], s[74:75], v[140:141], v[30:31] op_sel_hi:[0,1,1]
	v_pk_fma_f32 v[28:29], s[74:75], v[142:143], v[28:29] op_sel_hi:[0,1,1]
	v_cvt_scalef32_pk_f32_fp4 v[136:137], v133, 1.0
	v_cvt_scalef32_pk_f32_fp4 v[138:139], v133, 1.0 op_sel:[1,0,0]
	v_cvt_scalef32_pk_f32_fp4 v[140:141], v133, 1.0 op_sel:[0,1,0]
	v_cvt_scalef32_pk_f32_fp4 v[142:143], v133, 1.0 op_sel:[1,1,0]
	v_pk_fma_f32 v[26:27], s[74:75], v[136:137], v[26:27] op_sel_hi:[0,1,1]
	v_pk_fma_f32 v[24:25], s[74:75], v[138:139], v[24:25] op_sel_hi:[0,1,1]
	v_pk_fma_f32 v[20:21], s[74:75], v[140:141], v[20:21] op_sel_hi:[0,1,1]
	v_pk_fma_f32 v[22:23], s[74:75], v[142:143], v[22:23] op_sel_hi:[0,1,1]
	s_waitcnt vmcnt(0)
; DI void peer_token(LAS unsigned char* ring, const bf16* x1row, float inv2, const float* nffn, const int* ex, const float* pg, const unsigned char* U6, const unsigned char* V6,
;                    const float* usc, const float* vsc, float* orow, int lane) {
;     ...
;     asm volatile("s_waitcnt vmcnt(0)" ::: "memory");
; #pragma unroll
;     for (int i = 0; i < 16; ++i) {
;         const v2u aw = *(const v2u*)(x1row + i * 256 + lane * 4);
;         *(f32x4*)(orow + i * 256 + lane * 4) = (f32x4){bflo(aw.x) + ysc * y[2 * i].x, bfhi(aw.x) + ysc * y[2 * i].y, bflo(aw.y) + ysc * y[2 * i + 1].x, bfhi(aw.y) + ysc * y[2 * i + 1].y};
;     }
; __global__ void __launch_bounds__(NTHREADS, 2) fwd(Args args) {
;     ...
;         for (int tb = bid; tb < SEQ / 32; tb += G) {
;             routing_block(lds, QB, skb, experts, pgates, tb);
;             asm volatile("s_waitcnt vmcnt(0)" ::: "memory");
;             __syncthreads();
; #pragma unroll 1
;             for (int j = 0; j < 4; ++j) { const int t = tb * 32 + wave * 4 + j;
;                 peer_token(lds + wave * (4 * RSLOT), XB + (size_t)t * DM, inv2[t], norm_ffn, experts + (size_t)t * 128, pgates + (size_t)t * 128, U8, V8, usc, vsc, out + (size_t)t * DM, lane); }
;             __syncthreads();
	v_lshl_add_u64 v[98:99], s[44:45], 2, v[76:77]
	s_add_i32 s76, s76, 1
	s_cmp_eq_u32 s76, 4
	v_add_co_u32_e32 v100, vcc, s81, v98
	s_nop 1
	v_addc_co_u32_e32 v101, vcc, 0, v99, vcc
	v_add_co_u32_e32 v102, vcc, s84, v98
	s_nop 1
	v_addc_co_u32_e32 v103, vcc, 0, v99, vcc
	v_lshlrev_b32_e32 v2, 16, v146
	v_and_b32_e32 v3, 0xffff0000, v146
	v_lshlrev_b32_e32 v4, 16, v147
	v_and_b32_e32 v5, 0xffff0000, v147
	v_pk_add_f32 v[2:3], v[94:95], v[2:3]
	v_pk_add_f32 v[4:5], v[96:97], v[4:5]
	global_store_dwordx4 v[98:99], v[2:5], off
	v_lshlrev_b32_e32 v10, 16, v148
	v_and_b32_e32 v11, 0xffff0000, v148
	v_lshlrev_b32_e32 v12, 16, v149
	v_and_b32_e32 v13, 0xffff0000, v149
	v_pk_add_f32 v[10:11], v[92:93], v[10:11]
	v_pk_add_f32 v[12:13], v[90:91], v[12:13]
	global_store_dwordx4 v[98:99], v[10:13], off offset:1024
	v_lshlrev_b32_e32 v14, 16, v150
	v_and_b32_e32 v15, 0xffff0000, v150
	v_lshlrev_b32_e32 v16, 16, v151
	v_and_b32_e32 v17, 0xffff0000, v151
	v_pk_add_f32 v[14:15], v[88:89], v[14:15]
	v_pk_add_f32 v[16:17], v[86:87], v[16:17]
	global_store_dwordx4 v[98:99], v[14:17], off offset:2048
	v_lshlrev_b32_e32 v2, 16, v152
	v_and_b32_e32 v3, 0xffff0000, v152
	v_lshlrev_b32_e32 v4, 16, v153
	v_and_b32_e32 v5, 0xffff0000, v153
	v_pk_add_f32 v[2:3], v[84:85], v[2:3]
	v_pk_add_f32 v[4:5], v[82:83], v[4:5]
	global_store_dwordx4 v[98:99], v[2:5], off offset:3072
	v_lshlrev_b32_e32 v10, 16, v154
	v_and_b32_e32 v11, 0xffff0000, v154
	v_lshlrev_b32_e32 v12, 16, v155
	v_and_b32_e32 v13, 0xffff0000, v155
	v_pk_add_f32 v[10:11], v[64:65], v[10:11]
	v_pk_add_f32 v[12:13], v[80:81], v[12:13]
	global_store_dwordx4 v[100:101], v[10:13], off offset:-4096
	v_lshlrev_b32_e32 v14, 16, v156
	v_and_b32_e32 v15, 0xffff0000, v156
	v_lshlrev_b32_e32 v16, 16, v157
	v_and_b32_e32 v17, 0xffff0000, v157
	v_pk_add_f32 v[14:15], v[62:63], v[14:15]
	v_pk_add_f32 v[16:17], v[60:61], v[16:17]
	global_store_dwordx4 v[100:101], v[14:17], off offset:-3072
	v_lshlrev_b32_e32 v2, 16, v158
	v_and_b32_e32 v3, 0xffff0000, v158
	v_lshlrev_b32_e32 v4, 16, v159
	v_and_b32_e32 v5, 0xffff0000, v159
	v_pk_add_f32 v[2:3], v[58:59], v[2:3]
	v_pk_add_f32 v[4:5], v[56:57], v[4:5]
	global_store_dwordx4 v[100:101], v[2:5], off offset:-2048
	v_lshlrev_b32_e32 v10, 16, v160
	v_and_b32_e32 v11, 0xffff0000, v160
	v_lshlrev_b32_e32 v12, 16, v161
	v_and_b32_e32 v13, 0xffff0000, v161
	v_pk_add_f32 v[10:11], v[54:55], v[10:11]
	v_pk_add_f32 v[12:13], v[52:53], v[12:13]
	global_store_dwordx4 v[100:101], v[10:13], off offset:-1024
	v_lshlrev_b32_e32 v14, 16, v162
	v_and_b32_e32 v15, 0xffff0000, v162
	v_lshlrev_b32_e32 v16, 16, v163
	v_and_b32_e32 v17, 0xffff0000, v163
	v_pk_add_f32 v[14:15], v[50:51], v[14:15]
	v_pk_add_f32 v[16:17], v[48:49], v[16:17]
	global_store_dwordx4 v[100:101], v[14:17], off
	v_lshlrev_b32_e32 v2, 16, v164
	v_and_b32_e32 v3, 0xffff0000, v164
	v_lshlrev_b32_e32 v4, 16, v165
	v_and_b32_e32 v5, 0xffff0000, v165
	v_pk_add_f32 v[2:3], v[46:47], v[2:3]
	v_pk_add_f32 v[4:5], v[44:45], v[4:5]
	global_store_dwordx4 v[100:101], v[2:5], off offset:1024
	v_lshlrev_b32_e32 v10, 16, v166
	v_and_b32_e32 v11, 0xffff0000, v166
	v_lshlrev_b32_e32 v12, 16, v167
	v_and_b32_e32 v13, 0xffff0000, v167
	v_pk_add_f32 v[10:11], v[42:43], v[10:11]
	v_pk_add_f32 v[12:13], v[40:41], v[12:13]
	global_store_dwordx4 v[100:101], v[10:13], off offset:2048
	v_lshlrev_b32_e32 v14, 16, v168
	v_and_b32_e32 v15, 0xffff0000, v168
	v_lshlrev_b32_e32 v16, 16, v169
	v_and_b32_e32 v17, 0xffff0000, v169
	v_pk_add_f32 v[14:15], v[38:39], v[14:15]
	v_pk_add_f32 v[16:17], v[36:37], v[16:17]
	global_store_dwordx4 v[100:101], v[14:17], off offset:3072
	v_lshlrev_b32_e32 v2, 16, v170
	v_and_b32_e32 v3, 0xffff0000, v170
	v_lshlrev_b32_e32 v4, 16, v171
	v_and_b32_e32 v5, 0xffff0000, v171
	v_pk_add_f32 v[2:3], v[32:33], v[2:3]
	v_pk_add_f32 v[4:5], v[34:35], v[4:5]
	global_store_dwordx4 v[102:103], v[2:5], off
	v_lshlrev_b32_e32 v10, 16, v172
	v_and_b32_e32 v11, 0xffff0000, v172
	v_lshlrev_b32_e32 v12, 16, v173
	v_and_b32_e32 v13, 0xffff0000, v173
	v_pk_add_f32 v[10:11], v[30:31], v[10:11]
	v_pk_add_f32 v[12:13], v[28:29], v[12:13]
	global_store_dwordx4 v[102:103], v[10:13], off offset:1024
	v_lshlrev_b32_e32 v14, 16, v174
	v_and_b32_e32 v15, 0xffff0000, v174
	v_lshlrev_b32_e32 v16, 16, v175
	v_and_b32_e32 v17, 0xffff0000, v175
	v_pk_add_f32 v[14:15], v[26:27], v[14:15]
	v_pk_add_f32 v[16:17], v[24:25], v[16:17]
	global_store_dwordx4 v[102:103], v[14:17], off offset:2048
	v_lshlrev_b32_e32 v2, 16, v176
	v_and_b32_e32 v3, 0xffff0000, v176
	v_lshlrev_b32_e32 v4, 16, v177
	v_and_b32_e32 v5, 0xffff0000, v177
	v_pk_add_f32 v[2:3], v[20:21], v[2:3]
	v_pk_add_f32 v[4:5], v[22:23], v[4:5]
	global_store_dwordx4 v[102:103], v[2:5], off offset:3072
	s_cbranch_scc0 .LBB0_901
	s_add_i32 s2, s2, s3
	s_cmpk_gt_i32 s2, 0xff
	s_barrier
	s_cbranch_scc0 .LBB0_892
